# K-loops: LDS-DMA in saddr form (no VALU address adds), one invariant B-fragment base; s_setprio and redundant lgkmcnt wait moved off barrier-to-MFMA path
# speedup vs baseline: 1.0171x; 1.0162x over previous
; #define PG8_STAGE(bufoff, gbase, voff) do { _Pragma("unroll") for (int _i = 0; _i < 2; ++_i) \
;         __builtin_amdgcn_global_load_lds((const unsigned*)((const char*)(gbase) + (voff)[_i]), (PG8_LAS unsigned*)(lds + (bufoff) + ldsw + _i * 8192), 16, 0, 0); } while (0)
; #define PG8_LDA(dst, b, h) do { _Pragma("unroll") for (int m = 0; m < 4; ++m) _Pragma("unroll") for (int k = 0; k < 2; ++k) dst[m][k] = *(const PG8_LAS bf16x8*)(lds + PG8_SA(b, h) + aoff + m * 2048 + k * 1024); } while (0)
; #define PG8_LDB(dst, b, h) do { _Pragma("unroll") for (int n = 0; n < 2; ++n) _Pragma("unroll") for (int k = 0; k < 2; ++k) dst[n][k] = *(const PG8_LAS bf16x8*)(lds + PG8_SB(b, h) + boff + n * 2048 + k * 1024); } while (0)
; #define PG8_WAIT_V(n) asm volatile("s_waitcnt vmcnt(" #n ")" ::: "memory")
; #define PG8_WAIT_L(n) asm volatile("s_waitcnt lgkmcnt(" #n ")" ::: "memory")
; #define PG8_BAR __builtin_amdgcn_s_barrier()
; #define PG8_SCHED __builtin_amdgcn_sched_barrier(0)
; template <class Epi, class Sched, bool ALIGN_EPI>
; __device__ __forceinline__ void gemm_phase(PG8_LAS unsigned char* lds, const Gemm g, const Sched& S, const Epi& E, const int tid) {
;     ...
;         const bool has_next = S.next(ui + 1, nxt);
;         const char* nA = has_next ? (const char*)g.A + (size_t)nxt.pm * tstepA + PG8_ACOL(nxt) : cA; const char* nB = has_next ? (const char*)g.Bt + (size_t)nxt.pn * tstepB : cB;
;         for (int t = 0; t < nt; t += 2) {
;             const bool last = (t == nt - 2);
;             const char* a1 = cA + (size_t)(t + 1) * kstepA;
;             const char* a2 = last ? nA : cA + (size_t)(t + 2) * kstepA; const char* b2 = last ? nB : cB + (size_t)(t + 2) * kstepB;
;             const char* a3 = a2 + kstepA; const char* b3 = b2 + kstepB;
;             if (last && has_next) S.a_ready(nxt);
;             PG8_LDB(B0, 0, 0); PG8_LDB(B1, 0, 1); PG8_SCHED; PG8_LDA(At, 0, 0); PG8_STAGE(PG8_SA(1, 1), a1 + hstepA, voffA);
;             PG8_WAIT_V(8); PG8_WAIT_L(0); PG8_BAR; PG8_MMA(0, 0, At, B0); PG8_MMA(0, 1, At, B1); PG8_BAR; PG8_SCHED;
;     ...
; #pragma unroll
;         for (int a = 0; a < 2; ++a)
; #pragma unroll
;             for (int b = 0; b < 2; ++b)
; #pragma unroll
;                 for (int m = 0; m < 4; ++m)
; #pragma unroll
;                     for (int n = 0; n < 2; ++n) acc[a][b][m][n] = (f32x4){0.f, 0.f, 0.f, 0.f};
.LBB0_245:
	s_ashr_i32 s11, s10, 31
	s_lshl_b64 s[12:13], s[10:11], 20
	s_add_u32 s12, s43, s12
	s_addc_u32 s13, s44, s13
	s_and_b64 s[14:15], s[2:3], exec
	s_cselect_b32 s11, s13, s17
	s_cselect_b32 s58, s12, s16
	s_ashr_i32 s9, s8, 31
	s_lshl_b64 s[14:15], s[8:9], 20
	s_add_u32 s14, s40, s14
	s_addc_u32 s15, s41, s15
	s_and_b64 s[20:21], s[2:3], exec
	s_cselect_b32 s9, s15, s19
	s_cselect_b32 s59, s14, s18
	s_add_u32 s16, s16, 0xc000
	s_addc_u32 s17, s17, 0
	s_add_u32 s60, s18, 0x10000
	v_mov_b32_e32 v0, 0
	s_addc_u32 s61, s19, 0
	s_mov_b32 s62, -2
	v_mov_b32_e32 v1, v0
	v_mov_b32_e32 v2, v0
	v_mov_b32_e32 v3, v0
	v_mov_b32_e32 v8, v0
	v_mov_b32_e32 v9, v0
	v_mov_b32_e32 v10, v0
	v_mov_b32_e32 v11, v0
	v_mov_b32_e32 v16, v0
	v_mov_b32_e32 v17, v0
	v_mov_b32_e32 v18, v0
	v_mov_b32_e32 v19, v0
	v_mov_b32_e32 v24, v0
	v_mov_b32_e32 v25, v0
	v_mov_b32_e32 v26, v0
	v_mov_b32_e32 v27, v0
	v_mov_b32_e32 v32, v0
	v_mov_b32_e32 v33, v0
	v_mov_b32_e32 v34, v0
	v_mov_b32_e32 v35, v0
	v_mov_b32_e32 v40, v0
	v_mov_b32_e32 v41, v0
	v_mov_b32_e32 v42, v0
	v_mov_b32_e32 v43, v0
	v_mov_b32_e32 v48, v0
	v_mov_b32_e32 v49, v0
	v_mov_b32_e32 v50, v0
	v_mov_b32_e32 v51, v0
	v_mov_b32_e32 v56, v0
	v_mov_b32_e32 v57, v0
	v_mov_b32_e32 v58, v0
	v_mov_b32_e32 v59, v0
	v_mov_b32_e32 v4, v0
	v_mov_b32_e32 v5, v0
	v_mov_b32_e32 v6, v0
	v_mov_b32_e32 v7, v0
	v_mov_b32_e32 v12, v0
	v_mov_b32_e32 v13, v0
	v_mov_b32_e32 v14, v0
	v_mov_b32_e32 v15, v0
	v_mov_b32_e32 v20, v0
	v_mov_b32_e32 v21, v0
	v_mov_b32_e32 v22, v0
	v_mov_b32_e32 v23, v0
	v_mov_b32_e32 v28, v0
	v_mov_b32_e32 v29, v0
	v_mov_b32_e32 v30, v0
	v_mov_b32_e32 v31, v0
	v_mov_b32_e32 v36, v0
	v_mov_b32_e32 v37, v0
	v_mov_b32_e32 v38, v0
	v_mov_b32_e32 v39, v0
	v_mov_b32_e32 v44, v0
	v_mov_b32_e32 v45, v0
	v_mov_b32_e32 v46, v0
	v_mov_b32_e32 v47, v0
	v_mov_b32_e32 v52, v0
	v_mov_b32_e32 v53, v0
	v_mov_b32_e32 v54, v0
	v_mov_b32_e32 v55, v0
	v_mov_b32_e32 v60, v0
	v_mov_b32_e32 v61, v0
	v_mov_b32_e32 v62, v0
	v_mov_b32_e32 v63, v0
	v_mov_b32_e32 v64, v0
	v_mov_b32_e32 v65, v0
	v_mov_b32_e32 v66, v0
	v_mov_b32_e32 v67, v0
	v_mov_b32_e32 v72, v0
	v_mov_b32_e32 v73, v0
	v_mov_b32_e32 v74, v0
	v_mov_b32_e32 v75, v0
	v_mov_b32_e32 v88, v0
	v_mov_b32_e32 v89, v0
	v_mov_b32_e32 v90, v0
	v_mov_b32_e32 v91, v0
	v_mov_b32_e32 v104, v0
	v_mov_b32_e32 v105, v0
	v_mov_b32_e32 v106, v0
	v_mov_b32_e32 v107, v0
	v_mov_b32_e32 v112, v0
	v_mov_b32_e32 v113, v0
	v_mov_b32_e32 v114, v0
	v_mov_b32_e32 v115, v0
	v_mov_b32_e32 v120, v0
	v_mov_b32_e32 v121, v0
	v_mov_b32_e32 v122, v0
	v_mov_b32_e32 v123, v0
	v_mov_b32_e32 v130, v0
	v_mov_b32_e32 v131, v0
	v_mov_b32_e32 v132, v0
	v_mov_b32_e32 v133, v0
	v_mov_b32_e32 v138, v0
	v_mov_b32_e32 v139, v0
	v_mov_b32_e32 v140, v0
	v_mov_b32_e32 v141, v0
	v_mov_b32_e32 v68, v0
	v_mov_b32_e32 v69, v0
	v_mov_b32_e32 v70, v0
	v_mov_b32_e32 v71, v0
	v_mov_b32_e32 v76, v0
	v_mov_b32_e32 v77, v0
	v_mov_b32_e32 v78, v0
	v_mov_b32_e32 v79, v0
	v_mov_b32_e32 v92, v0
	v_mov_b32_e32 v93, v0
	v_mov_b32_e32 v94, v0
	v_mov_b32_e32 v95, v0
	v_mov_b32_e32 v108, v0
	v_mov_b32_e32 v109, v0
	v_mov_b32_e32 v110, v0
	v_mov_b32_e32 v111, v0
	v_mov_b32_e32 v116, v0
	v_mov_b32_e32 v117, v0
	v_mov_b32_e32 v118, v0
	v_mov_b32_e32 v119, v0
	v_mov_b32_e32 v124, v0
	v_mov_b32_e32 v125, v0
	v_mov_b32_e32 v126, v0
	v_mov_b32_e32 v127, v0
	v_mov_b32_e32 v134, v0
	v_mov_b32_e32 v135, v0
	v_mov_b32_e32 v136, v0
	v_mov_b32_e32 v137, v0
	v_mov_b32_e32 v142, v0
	v_mov_b32_e32 v143, v0
	v_mov_b32_e32 v144, v0
	v_mov_b32_e32 v145, v0
	v_add_u32_e32 v166, 0x10000, v178
.LBB0_246:
	s_add_u32 s18, s16, 0x4000
	s_addc_u32 s19, s17, 0
	s_cmp_eq_u32 s62, 28
	s_cselect_b32 s22, s58, s18
	s_cselect_b32 s23, s11, s19
	s_cselect_b32 s20, s59, s60
	s_cselect_b32 s21, s9, s61
	s_add_u32 s18, s22, 0x8000
	s_addc_u32 s19, s23, 0
	s_add_i32 s63, 0, 0x10000
	s_add_i32 s66, 0, 0x14000
	ds_read_b128 v[80:83], v166
	ds_read_b128 v[84:87], v166 offset:1024
	ds_read_b128 v[96:99], v166 offset:2048
	ds_read_b128 v[100:103], v166 offset:3072
	ds_read_b128 v[162:165], v166 offset:16384
	ds_read_b128 v[182:185], v166 offset:17408
	ds_read_b128 v[186:189], v166 offset:18432
	ds_read_b128 v[190:193], v166 offset:19456
	s_add_i32 m0, s45, 0xc000
	ds_read_b128 v[194:197], v180
	ds_read_b128 v[198:201], v180 offset:1024
	ds_read_b128 v[202:205], v180 offset:2048
	ds_read_b128 v[206:209], v180 offset:3072
	ds_read_b128 v[210:213], v180 offset:4096
	ds_read_b128 v[214:217], v180 offset:5120
	ds_read_b128 v[218:221], v180 offset:6144
	ds_read_b128 v[222:225], v180 offset:7168
	global_load_lds_dwordx4 v158, s[16:17]
	s_add_i32 m0, s45, 0xe000
	s_nop 0
	global_load_lds_dwordx4 v160, s[16:17]
	s_waitcnt vmcnt(8)
	s_waitcnt lgkmcnt(0)
	s_setprio 1
	s_barrier
; #define PG8_STAGE(bufoff, gbase, voff) do { _Pragma("unroll") for (int _i = 0; _i < 2; ++_i) \
;         __builtin_amdgcn_global_load_lds((const unsigned*)((const char*)(gbase) + (voff)[_i]), (PG8_LAS unsigned*)(lds + (bufoff) + ldsw + _i * 8192), 16, 0, 0); } while (0)
; #define PG8_LDA(dst, b, h) do { _Pragma("unroll") for (int m = 0; m < 4; ++m) _Pragma("unroll") for (int k = 0; k < 2; ++k) dst[m][k] = *(const PG8_LAS bf16x8*)(lds + PG8_SA(b, h) + aoff + m * 2048 + k * 1024); } while (0)
; #define PG8_MMA(ai, bj, At, Bt) do { __builtin_amdgcn_s_setprio(1); _Pragma("unroll") for (int m = 0; m < 4; ++m) _Pragma("unroll") for (int n = 0; n < 2; ++n) _Pragma("unroll") for (int k = 0; k < 2; ++k) \
;         acc[ai][bj][m][n] = __builtin_amdgcn_mfma_f32_16x16x32_bf16(Bt[n][k], At[m][k], acc[ai][bj][m][n], 0, 0, 0); __builtin_amdgcn_s_setprio(0); } while (0)
; #define PG8_WAIT_V(n) asm volatile("s_waitcnt vmcnt(" #n ")" ::: "memory")
; #define PG8_WAIT_L(n) asm volatile("s_waitcnt lgkmcnt(" #n ")" ::: "memory")
; #define PG8_BAR __builtin_amdgcn_s_barrier()
; #define PG8_SCHED __builtin_amdgcn_sched_barrier(0)
; template <class Epi, class Sched, bool ALIGN_EPI>
; __device__ __forceinline__ void gemm_phase(PG8_LAS unsigned char* lds, const Gemm g, const Sched& S, const Epi& E, const int tid) {
;     ...
;             PG8_WAIT_V(8); PG8_WAIT_L(0); PG8_BAR; PG8_MMA(0, 0, At, B0); PG8_MMA(0, 1, At, B1); PG8_BAR; PG8_SCHED;
;             PG8_LDA(At, 0, 1); PG8_STAGE(PG8_SB(0, 0), b2, voffB); PG8_STAGE(PG8_SB(0, 1), b2 + hstepB, voffB); PG8_STAGE(PG8_SA(0, 0), a2, voffA);
;             PG8_WAIT_V(8); PG8_WAIT_L(0); PG8_BAR; PG8_MMA(1, 0, At, B0); PG8_MMA(1, 1, At, B1); PG8_BAR; PG8_SCHED;
	v_mfma_f32_16x16x32_bf16 v[142:145], v[80:83], v[194:197], v[142:145]
	v_mfma_f32_16x16x32_bf16 v[134:137], v[96:99], v[194:197], v[134:137]
	v_mfma_f32_16x16x32_bf16 v[124:127], v[80:83], v[202:205], v[124:127]
	v_mfma_f32_16x16x32_bf16 v[116:119], v[96:99], v[202:205], v[116:119]
	v_mfma_f32_16x16x32_bf16 v[108:111], v[80:83], v[210:213], v[108:111]
	v_mfma_f32_16x16x32_bf16 v[92:95], v[96:99], v[210:213], v[92:95]
	v_mfma_f32_16x16x32_bf16 v[76:79], v[80:83], v[218:221], v[76:79]
	v_mfma_f32_16x16x32_bf16 v[68:71], v[96:99], v[218:221], v[68:71]
	v_mfma_f32_16x16x32_bf16 v[142:145], v[84:87], v[198:201], v[142:145]
	v_mfma_f32_16x16x32_bf16 v[134:137], v[100:103], v[198:201], v[134:137]
	v_mfma_f32_16x16x32_bf16 v[124:127], v[84:87], v[206:209], v[124:127]
	v_mfma_f32_16x16x32_bf16 v[116:119], v[100:103], v[206:209], v[116:119]
	v_mfma_f32_16x16x32_bf16 v[108:111], v[84:87], v[214:217], v[108:111]
	v_mfma_f32_16x16x32_bf16 v[92:95], v[100:103], v[214:217], v[92:95]
	v_mfma_f32_16x16x32_bf16 v[76:79], v[84:87], v[222:225], v[76:79]
	v_mfma_f32_16x16x32_bf16 v[68:71], v[100:103], v[222:225], v[68:71]
	v_mfma_f32_16x16x32_bf16 v[138:141], v[162:165], v[194:197], v[138:141]
	v_mfma_f32_16x16x32_bf16 v[130:133], v[186:189], v[194:197], v[130:133]
	v_mfma_f32_16x16x32_bf16 v[120:123], v[162:165], v[202:205], v[120:123]
	v_mfma_f32_16x16x32_bf16 v[112:115], v[186:189], v[202:205], v[112:115]
	v_mfma_f32_16x16x32_bf16 v[104:107], v[162:165], v[210:213], v[104:107]
	v_mfma_f32_16x16x32_bf16 v[88:91], v[186:189], v[210:213], v[88:91]
	v_mfma_f32_16x16x32_bf16 v[72:75], v[162:165], v[218:221], v[72:75]
	v_mfma_f32_16x16x32_bf16 v[64:67], v[186:189], v[218:221], v[64:67]
	v_mfma_f32_16x16x32_bf16 v[138:141], v[182:185], v[198:201], v[138:141]
	v_mfma_f32_16x16x32_bf16 v[130:133], v[190:193], v[198:201], v[130:133]
	v_mfma_f32_16x16x32_bf16 v[120:123], v[182:185], v[206:209], v[120:123]
	v_mfma_f32_16x16x32_bf16 v[112:115], v[190:193], v[206:209], v[112:115]
	v_mfma_f32_16x16x32_bf16 v[104:107], v[182:185], v[214:217], v[104:107]
	v_mfma_f32_16x16x32_bf16 v[88:91], v[190:193], v[214:217], v[88:91]
	v_mfma_f32_16x16x32_bf16 v[72:75], v[182:185], v[222:225], v[72:75]
	v_mfma_f32_16x16x32_bf16 v[64:67], v[190:193], v[222:225], v[64:67]
	s_barrier
	s_setprio 0
	s_add_i32 s63, s63, s42
	s_mov_b32 m0, s63
	ds_read_b128 v[194:197], v180 offset:16384
	ds_read_b128 v[198:201], v180 offset:17408
	ds_read_b128 v[202:205], v180 offset:18432
	ds_read_b128 v[206:209], v180 offset:19456
	ds_read_b128 v[210:213], v180 offset:20480
	ds_read_b128 v[214:217], v180 offset:21504
	ds_read_b128 v[218:221], v180 offset:22528
	ds_read_b128 v[222:225], v180 offset:23552
	global_load_lds_dwordx4 v150, s[20:21]
	s_add_i32 m0, s63, 0x2000
	s_add_u32 s64, s20, 0x4000
	s_addc_u32 s65, s21, 0
	s_add_i32 s63, s66, s42
	global_load_lds_dwordx4 v146, s[20:21]
	s_mov_b32 m0, s63
	s_nop 0
	global_load_lds_dwordx4 v150, s[64:65]
	s_add_i32 m0, s63, 0x2000
	s_nop 0
	global_load_lds_dwordx4 v146, s[64:65]
	s_mov_b32 m0, s45
	s_nop 0
	global_load_lds_dwordx4 v152, s[22:23]
	s_mov_b32 m0, s46
	s_nop 0
	global_load_lds_dwordx4 v148, s[22:23]
	s_waitcnt vmcnt(8)
	s_waitcnt lgkmcnt(0)
	s_setprio 1
	s_barrier
	v_mfma_f32_16x16x32_bf16 v[60:63], v[80:83], v[194:197], v[60:63]
	v_mfma_f32_16x16x32_bf16 v[52:55], v[96:99], v[194:197], v[52:55]
	v_mfma_f32_16x16x32_bf16 v[44:47], v[80:83], v[202:205], v[44:47]
	v_mfma_f32_16x16x32_bf16 v[36:39], v[96:99], v[202:205], v[36:39]
	v_mfma_f32_16x16x32_bf16 v[28:31], v[80:83], v[210:213], v[28:31]
	v_mfma_f32_16x16x32_bf16 v[20:23], v[96:99], v[210:213], v[20:23]
	v_mfma_f32_16x16x32_bf16 v[12:15], v[80:83], v[218:221], v[12:15]
	v_mfma_f32_16x16x32_bf16 v[4:7], v[96:99], v[218:221], v[4:7]
	v_mfma_f32_16x16x32_bf16 v[60:63], v[84:87], v[198:201], v[60:63]
	v_mfma_f32_16x16x32_bf16 v[52:55], v[100:103], v[198:201], v[52:55]
	v_mfma_f32_16x16x32_bf16 v[44:47], v[84:87], v[206:209], v[44:47]
	v_mfma_f32_16x16x32_bf16 v[36:39], v[100:103], v[206:209], v[36:39]
	v_mfma_f32_16x16x32_bf16 v[28:31], v[84:87], v[214:217], v[28:31]
	v_mfma_f32_16x16x32_bf16 v[20:23], v[100:103], v[214:217], v[20:23]
	v_mfma_f32_16x16x32_bf16 v[12:15], v[84:87], v[222:225], v[12:15]
	v_mfma_f32_16x16x32_bf16 v[4:7], v[100:103], v[222:225], v[4:7]
	v_mfma_f32_16x16x32_bf16 v[56:59], v[162:165], v[194:197], v[56:59]
	v_mfma_f32_16x16x32_bf16 v[48:51], v[186:189], v[194:197], v[48:51]
	v_mfma_f32_16x16x32_bf16 v[40:43], v[162:165], v[202:205], v[40:43]
	v_mfma_f32_16x16x32_bf16 v[32:35], v[186:189], v[202:205], v[32:35]
	v_mfma_f32_16x16x32_bf16 v[24:27], v[162:165], v[210:213], v[24:27]
	v_mfma_f32_16x16x32_bf16 v[16:19], v[186:189], v[210:213], v[16:19]
	v_mfma_f32_16x16x32_bf16 v[8:11], v[162:165], v[218:221], v[8:11]
	v_mfma_f32_16x16x32_bf16 v[0:3], v[186:189], v[218:221], v[0:3]
	v_mfma_f32_16x16x32_bf16 v[56:59], v[182:185], v[198:201], v[56:59]
	v_mfma_f32_16x16x32_bf16 v[48:51], v[190:193], v[198:201], v[48:51]
	v_mfma_f32_16x16x32_bf16 v[40:43], v[182:185], v[206:209], v[40:43]
	v_mfma_f32_16x16x32_bf16 v[32:35], v[190:193], v[206:209], v[32:35]
	v_mfma_f32_16x16x32_bf16 v[24:27], v[182:185], v[214:217], v[24:27]
	v_mfma_f32_16x16x32_bf16 v[16:19], v[190:193], v[214:217], v[16:19]
	v_mfma_f32_16x16x32_bf16 v[8:11], v[182:185], v[222:225], v[8:11]
	v_mfma_f32_16x16x32_bf16 v[0:3], v[190:193], v[222:225], v[0:3]
	s_barrier
; #define PG8_STAGE(bufoff, gbase, voff) do { _Pragma("unroll") for (int _i = 0; _i < 2; ++_i) \
;         __builtin_amdgcn_global_load_lds((const unsigned*)((const char*)(gbase) + (voff)[_i]), (PG8_LAS unsigned*)(lds + (bufoff) + ldsw + _i * 8192), 16, 0, 0); } while (0)
; #define PG8_LDA(dst, b, h) do { _Pragma("unroll") for (int m = 0; m < 4; ++m) _Pragma("unroll") for (int k = 0; k < 2; ++k) dst[m][k] = *(const PG8_LAS bf16x8*)(lds + PG8_SA(b, h) + aoff + m * 2048 + k * 1024); } while (0)
; #define PG8_LDB(dst, b, h) do { _Pragma("unroll") for (int n = 0; n < 2; ++n) _Pragma("unroll") for (int k = 0; k < 2; ++k) dst[n][k] = *(const PG8_LAS bf16x8*)(lds + PG8_SB(b, h) + boff + n * 2048 + k * 1024); } while (0)
; #define PG8_MMA(ai, bj, At, Bt) do { __builtin_amdgcn_s_setprio(1); _Pragma("unroll") for (int m = 0; m < 4; ++m) _Pragma("unroll") for (int n = 0; n < 2; ++n) _Pragma("unroll") for (int k = 0; k < 2; ++k) \
;         acc[ai][bj][m][n] = __builtin_amdgcn_mfma_f32_16x16x32_bf16(Bt[n][k], At[m][k], acc[ai][bj][m][n], 0, 0, 0); __builtin_amdgcn_s_setprio(0); } while (0)
; #define PG8_WAIT_V(n) asm volatile("s_waitcnt vmcnt(" #n ")" ::: "memory")
; #define PG8_WAIT_L(n) asm volatile("s_waitcnt lgkmcnt(" #n ")" ::: "memory")
; #define PG8_BAR __builtin_amdgcn_s_barrier()
; #define PG8_SCHED __builtin_amdgcn_sched_barrier(0)
; template <class Epi, class Sched, bool ALIGN_EPI>
; __device__ __forceinline__ void gemm_phase(PG8_LAS unsigned char* lds, const Gemm g, const Sched& S, const Epi& E, const int tid) {
;     ...
;             PG8_LDB(B0, 1, 0); PG8_LDB(B1, 1, 1); PG8_SCHED; PG8_LDA(At, 1, 0); PG8_STAGE(PG8_SA(0, 1), a2 + hstepA, voffA);
;             PG8_WAIT_V(8); PG8_WAIT_L(0); PG8_BAR; PG8_MMA(0, 0, At, B0); PG8_MMA(0, 1, At, B1); PG8_BAR; PG8_SCHED;
;             PG8_LDA(At, 1, 1); PG8_STAGE(PG8_SB(1, 0), b3, voffB); PG8_STAGE(PG8_SB(1, 1), b3 + hstepB, voffB); PG8_STAGE(PG8_SA(1, 0), a3, voffA);
;             PG8_WAIT_V(8); PG8_WAIT_L(0); PG8_BAR; PG8_MMA(1, 0, At, B0); PG8_MMA(1, 1, At, B1); PG8_BAR; PG8_SCHED;
;         }
	s_setprio 0
	s_add_i32 s63, 0, 0x18000
	s_add_i32 s64, 0, 0x1c000
	ds_read_b128 v[80:83], v166 offset:32768
	ds_read_b128 v[84:87], v166 offset:33792
	ds_read_b128 v[96:99], v166 offset:34816
	ds_read_b128 v[100:103], v166 offset:35840
	ds_read_b128 v[162:165], v166 offset:49152
	ds_read_b128 v[182:185], v166 offset:50176
	ds_read_b128 v[186:189], v166 offset:51200
	ds_read_b128 v[190:193], v166 offset:52224
	s_add_u32 s22, s22, 0x4000
	s_addc_u32 s23, s23, 0
	s_mov_b32 m0, s47
	ds_read_b128 v[194:197], v180 offset:32768
	ds_read_b128 v[198:201], v180 offset:33792
	ds_read_b128 v[202:205], v180 offset:34816
	ds_read_b128 v[206:209], v180 offset:35840
	ds_read_b128 v[210:213], v180 offset:36864
	ds_read_b128 v[214:217], v180 offset:37888
	ds_read_b128 v[218:221], v180 offset:38912
	ds_read_b128 v[222:225], v180 offset:39936
	global_load_lds_dwordx4 v152, s[22:23]
	s_mov_b32 m0, s48
	s_nop 0
	global_load_lds_dwordx4 v148, s[22:23]
	s_waitcnt vmcnt(8)
	s_waitcnt lgkmcnt(0)
	s_setprio 1
	s_barrier
	v_mfma_f32_16x16x32_bf16 v[142:145], v[80:83], v[194:197], v[142:145]
	v_mfma_f32_16x16x32_bf16 v[134:137], v[96:99], v[194:197], v[134:137]
	v_mfma_f32_16x16x32_bf16 v[124:127], v[80:83], v[202:205], v[124:127]
	v_mfma_f32_16x16x32_bf16 v[116:119], v[96:99], v[202:205], v[116:119]
	v_mfma_f32_16x16x32_bf16 v[108:111], v[80:83], v[210:213], v[108:111]
	v_mfma_f32_16x16x32_bf16 v[92:95], v[96:99], v[210:213], v[92:95]
	v_mfma_f32_16x16x32_bf16 v[76:79], v[80:83], v[218:221], v[76:79]
	v_mfma_f32_16x16x32_bf16 v[68:71], v[96:99], v[218:221], v[68:71]
	v_mfma_f32_16x16x32_bf16 v[142:145], v[84:87], v[198:201], v[142:145]
	v_mfma_f32_16x16x32_bf16 v[134:137], v[100:103], v[198:201], v[134:137]
	v_mfma_f32_16x16x32_bf16 v[124:127], v[84:87], v[206:209], v[124:127]
	v_mfma_f32_16x16x32_bf16 v[116:119], v[100:103], v[206:209], v[116:119]
	v_mfma_f32_16x16x32_bf16 v[108:111], v[84:87], v[214:217], v[108:111]
	v_mfma_f32_16x16x32_bf16 v[92:95], v[100:103], v[214:217], v[92:95]
	v_mfma_f32_16x16x32_bf16 v[76:79], v[84:87], v[222:225], v[76:79]
	v_mfma_f32_16x16x32_bf16 v[68:71], v[100:103], v[222:225], v[68:71]
	v_mfma_f32_16x16x32_bf16 v[138:141], v[162:165], v[194:197], v[138:141]
	v_mfma_f32_16x16x32_bf16 v[130:133], v[186:189], v[194:197], v[130:133]
	v_mfma_f32_16x16x32_bf16 v[120:123], v[162:165], v[202:205], v[120:123]
	v_mfma_f32_16x16x32_bf16 v[112:115], v[186:189], v[202:205], v[112:115]
	v_mfma_f32_16x16x32_bf16 v[104:107], v[162:165], v[210:213], v[104:107]
	v_mfma_f32_16x16x32_bf16 v[88:91], v[186:189], v[210:213], v[88:91]
	v_mfma_f32_16x16x32_bf16 v[72:75], v[162:165], v[218:221], v[72:75]
	v_mfma_f32_16x16x32_bf16 v[64:67], v[186:189], v[218:221], v[64:67]
	v_mfma_f32_16x16x32_bf16 v[138:141], v[182:185], v[198:201], v[138:141]
	v_mfma_f32_16x16x32_bf16 v[130:133], v[190:193], v[198:201], v[130:133]
	v_mfma_f32_16x16x32_bf16 v[120:123], v[182:185], v[206:209], v[120:123]
	v_mfma_f32_16x16x32_bf16 v[112:115], v[190:193], v[206:209], v[112:115]
	v_mfma_f32_16x16x32_bf16 v[104:107], v[182:185], v[214:217], v[104:107]
	v_mfma_f32_16x16x32_bf16 v[88:91], v[190:193], v[214:217], v[88:91]
	v_mfma_f32_16x16x32_bf16 v[72:75], v[182:185], v[222:225], v[72:75]
	v_mfma_f32_16x16x32_bf16 v[64:67], v[190:193], v[222:225], v[64:67]
	s_barrier
	s_setprio 0
	s_add_u32 s22, s20, 0x8000
	s_addc_u32 s23, s21, 0
	s_add_i32 s63, s63, s42
	s_mov_b32 m0, s63
	ds_read_b128 v[194:197], v180 offset:49152
	ds_read_b128 v[198:201], v180 offset:50176
	ds_read_b128 v[202:205], v180 offset:51200
	ds_read_b128 v[206:209], v180 offset:52224
	ds_read_b128 v[210:213], v180 offset:53248
	ds_read_b128 v[214:217], v180 offset:54272
	ds_read_b128 v[218:221], v180 offset:55296
	ds_read_b128 v[222:225], v180 offset:56320
	global_load_lds_dwordx4 v150, s[22:23]
	s_add_i32 m0, s63, 0x2000
	s_add_u32 s20, s20, 0xc000
	s_addc_u32 s21, s21, 0
	global_load_lds_dwordx4 v146, s[22:23]
	s_add_i32 s22, s64, s42
	s_mov_b32 m0, s22
	s_nop 0
	global_load_lds_dwordx4 v150, s[20:21]
	s_add_i32 m0, s22, 0x2000
	s_nop 0
	global_load_lds_dwordx4 v146, s[20:21]
	s_mov_b32 m0, s51
	s_nop 0
	global_load_lds_dwordx4 v152, s[18:19]
	s_mov_b32 m0, s52
	s_nop 0
	global_load_lds_dwordx4 v148, s[18:19]
	s_waitcnt vmcnt(8)
	s_waitcnt lgkmcnt(0)
	s_setprio 1
	s_barrier
	v_mfma_f32_16x16x32_bf16 v[60:63], v[80:83], v[194:197], v[60:63]
	v_mfma_f32_16x16x32_bf16 v[52:55], v[96:99], v[194:197], v[52:55]
	v_mfma_f32_16x16x32_bf16 v[44:47], v[80:83], v[202:205], v[44:47]
	v_mfma_f32_16x16x32_bf16 v[36:39], v[96:99], v[202:205], v[36:39]
	v_mfma_f32_16x16x32_bf16 v[28:31], v[80:83], v[210:213], v[28:31]
	v_mfma_f32_16x16x32_bf16 v[20:23], v[96:99], v[210:213], v[20:23]
	v_mfma_f32_16x16x32_bf16 v[12:15], v[80:83], v[218:221], v[12:15]
	v_mfma_f32_16x16x32_bf16 v[4:7], v[96:99], v[218:221], v[4:7]
	v_mfma_f32_16x16x32_bf16 v[60:63], v[84:87], v[198:201], v[60:63]
	v_mfma_f32_16x16x32_bf16 v[52:55], v[100:103], v[198:201], v[52:55]
	v_mfma_f32_16x16x32_bf16 v[44:47], v[84:87], v[206:209], v[44:47]
	v_mfma_f32_16x16x32_bf16 v[36:39], v[100:103], v[206:209], v[36:39]
	v_mfma_f32_16x16x32_bf16 v[28:31], v[84:87], v[214:217], v[28:31]
	v_mfma_f32_16x16x32_bf16 v[20:23], v[100:103], v[214:217], v[20:23]
	v_mfma_f32_16x16x32_bf16 v[12:15], v[84:87], v[222:225], v[12:15]
	v_mfma_f32_16x16x32_bf16 v[4:7], v[100:103], v[222:225], v[4:7]
	v_mfma_f32_16x16x32_bf16 v[56:59], v[162:165], v[194:197], v[56:59]
	v_mfma_f32_16x16x32_bf16 v[48:51], v[186:189], v[194:197], v[48:51]
	v_mfma_f32_16x16x32_bf16 v[40:43], v[162:165], v[202:205], v[40:43]
	v_mfma_f32_16x16x32_bf16 v[32:35], v[186:189], v[202:205], v[32:35]
	v_mfma_f32_16x16x32_bf16 v[24:27], v[162:165], v[210:213], v[24:27]
	v_mfma_f32_16x16x32_bf16 v[16:19], v[186:189], v[210:213], v[16:19]
	v_mfma_f32_16x16x32_bf16 v[8:11], v[162:165], v[218:221], v[8:11]
	v_mfma_f32_16x16x32_bf16 v[0:3], v[186:189], v[218:221], v[0:3]
	v_mfma_f32_16x16x32_bf16 v[56:59], v[182:185], v[198:201], v[56:59]
	v_mfma_f32_16x16x32_bf16 v[48:51], v[190:193], v[198:201], v[48:51]
	v_mfma_f32_16x16x32_bf16 v[40:43], v[182:185], v[206:209], v[40:43]
	v_mfma_f32_16x16x32_bf16 v[32:35], v[190:193], v[206:209], v[32:35]
	v_mfma_f32_16x16x32_bf16 v[24:27], v[182:185], v[214:217], v[24:27]
	v_mfma_f32_16x16x32_bf16 v[16:19], v[190:193], v[214:217], v[16:19]
	v_mfma_f32_16x16x32_bf16 v[8:11], v[182:185], v[222:225], v[8:11]
	v_mfma_f32_16x16x32_bf16 v[0:3], v[190:193], v[222:225], v[0:3]
	s_barrier
	s_setprio 0
	s_add_i32 s62, s62, 2
	s_add_u32 s16, s16, 0x10000
	s_addc_u32 s17, s17, 0
	s_add_u32 s60, s60, 0x10000
	s_addc_u32 s61, s61, 0
	s_cmp_gt_u32 s62, 29
	s_cbranch_scc0 .LBB0_246
	s_and_b64 vcc, exec, s[6:7]
	s_cbranch_vccz .LBB0_249
	s_barrier

; #define PG8_STAGE(bufoff, gbase, voff) do { _Pragma("unroll") for (int _i = 0; _i < 2; ++_i) \
;         __builtin_amdgcn_global_load_lds((const unsigned*)((const char*)(gbase) + (voff)[_i]), (PG8_LAS unsigned*)(lds + (bufoff) + ldsw + _i * 8192), 16, 0, 0); } while (0)
; #define PG8_LDA(dst, b, h) do { _Pragma("unroll") for (int m = 0; m < 4; ++m) _Pragma("unroll") for (int k = 0; k < 2; ++k) dst[m][k] = *(const PG8_LAS bf16x8*)(lds + PG8_SA(b, h) + aoff + m * 2048 + k * 1024); } while (0)
; #define PG8_LDB(dst, b, h) do { _Pragma("unroll") for (int n = 0; n < 2; ++n) _Pragma("unroll") for (int k = 0; k < 2; ++k) dst[n][k] = *(const PG8_LAS bf16x8*)(lds + PG8_SB(b, h) + boff + n * 2048 + k * 1024); } while (0)
; #define PG8_WAIT_V(n) asm volatile("s_waitcnt vmcnt(" #n ")" ::: "memory")
; #define PG8_WAIT_L(n) asm volatile("s_waitcnt lgkmcnt(" #n ")" ::: "memory")
; #define PG8_BAR __builtin_amdgcn_s_barrier()
; #define PG8_SCHED __builtin_amdgcn_sched_barrier(0)
; template <class Epi, class Sched, bool ALIGN_EPI>
; __device__ __forceinline__ void gemm_phase(PG8_LAS unsigned char* lds, const Gemm g, const Sched& S, const Epi& E, const int tid) {
;     ...
;         const bool has_next = S.next(ui + 1, nxt);
;         const char* nA = has_next ? (const char*)g.A + (size_t)nxt.pm * tstepA + PG8_ACOL(nxt) : cA; const char* nB = has_next ? (const char*)g.Bt + (size_t)nxt.pn * tstepB : cB;
;         for (int t = 0; t < nt; t += 2) {
;             const bool last = (t == nt - 2);
;             const char* a1 = cA + (size_t)(t + 1) * kstepA;
;             const char* a2 = last ? nA : cA + (size_t)(t + 2) * kstepA; const char* b2 = last ? nB : cB + (size_t)(t + 2) * kstepB;
;             const char* a3 = a2 + kstepA; const char* b3 = b2 + kstepB;
;             if (last && has_next) S.a_ready(nxt);
;             PG8_LDB(B0, 0, 0); PG8_LDB(B1, 0, 1); PG8_SCHED; PG8_LDA(At, 0, 0); PG8_STAGE(PG8_SA(1, 1), a1 + hstepA, voffA);
;             PG8_WAIT_V(8); PG8_WAIT_L(0); PG8_BAR; PG8_MMA(0, 0, At, B0); PG8_MMA(0, 1, At, B1); PG8_BAR; PG8_SCHED;
;     ...
; #pragma unroll
;         for (int a = 0; a < 2; ++a)
; #pragma unroll
;             for (int b = 0; b < 2; ++b)
; #pragma unroll
;                 for (int m = 0; m < 4; ++m)
; #pragma unroll
;                     for (int n = 0; n < 2; ++n) acc[a][b][m][n] = (f32x4){0.f, 0.f, 0.f, 0.f};
.LBB0_341:
	s_ashr_i32 s47, s46, 31
	s_lshl_b64 s[48:49], s[46:47], 20
	s_add_u32 s48, s57, s48
	s_addc_u32 s49, s58, s49
	s_and_b64 s[50:51], s[6:7], exec
	s_cselect_b32 s9, s49, s11
	s_cselect_b32 s43, s48, s10
	s_ashr_i32 s45, s44, 31
	s_lshl_b64 s[50:51], s[44:45], 20
	s_add_u32 s50, s56, s50
	s_addc_u32 s51, s33, s51
	s_and_b64 s[52:53], s[6:7], exec
	s_cselect_b32 s45, s51, s13
	s_cselect_b32 s47, s50, s12
	s_add_u32 s10, s10, 0xc000
	s_addc_u32 s11, s11, 0
	s_add_u32 s79, s12, 0x10000
	v_mov_b32_e32 v0, 0
	s_addc_u32 s80, s13, 0
	s_mov_b32 s81, -2
	v_mov_b32_e32 v1, v0
	s_waitcnt lgkmcnt(0)
	v_mov_b32_e32 v2, v0
	v_mov_b32_e32 v3, v0
	v_mov_b32_e32 v4, v0
	v_mov_b32_e32 v5, v0
	v_mov_b32_e32 v6, v0
	v_mov_b32_e32 v7, v0
	v_mov_b32_e32 v16, v0
	v_mov_b32_e32 v17, v0
	v_mov_b32_e32 v18, v0
	v_mov_b32_e32 v19, v0
	v_mov_b32_e32 v20, v0
	v_mov_b32_e32 v21, v0
	v_mov_b32_e32 v22, v0
	v_mov_b32_e32 v23, v0
	v_mov_b32_e32 v32, v0
	v_mov_b32_e32 v33, v0
	v_mov_b32_e32 v34, v0
	v_mov_b32_e32 v35, v0
	v_mov_b32_e32 v36, v0
	v_mov_b32_e32 v37, v0
	v_mov_b32_e32 v38, v0
	v_mov_b32_e32 v39, v0
	v_mov_b32_e32 v56, v0
	v_mov_b32_e32 v57, v0
	v_mov_b32_e32 v58, v0
	v_mov_b32_e32 v59, v0
	v_mov_b32_e32 v60, v0
	v_mov_b32_e32 v61, v0
	v_mov_b32_e32 v62, v0
	v_mov_b32_e32 v63, v0
	v_mov_b32_e32 v8, v0
	v_mov_b32_e32 v9, v0
	v_mov_b32_e32 v10, v0
	v_mov_b32_e32 v11, v0
	v_mov_b32_e32 v12, v0
	v_mov_b32_e32 v13, v0
	v_mov_b32_e32 v14, v0
	v_mov_b32_e32 v15, v0
	v_mov_b32_e32 v24, v0
	v_mov_b32_e32 v25, v0
	v_mov_b32_e32 v26, v0
	v_mov_b32_e32 v27, v0
	v_mov_b32_e32 v28, v0
	v_mov_b32_e32 v29, v0
	v_mov_b32_e32 v30, v0
	v_mov_b32_e32 v31, v0
	v_mov_b32_e32 v40, v0
	v_mov_b32_e32 v41, v0
	v_mov_b32_e32 v42, v0
	v_mov_b32_e32 v43, v0
	v_mov_b32_e32 v44, v0
	v_mov_b32_e32 v45, v0
	v_mov_b32_e32 v46, v0
	v_mov_b32_e32 v47, v0
	v_mov_b32_e32 v72, v0
	v_mov_b32_e32 v73, v0
	v_mov_b32_e32 v74, v0
	v_mov_b32_e32 v75, v0
	v_mov_b32_e32 v76, v0
	v_mov_b32_e32 v77, v0
	v_mov_b32_e32 v78, v0
	v_mov_b32_e32 v79, v0
	v_mov_b32_e32 v80, v0
	v_mov_b32_e32 v81, v0
	v_mov_b32_e32 v82, v0
	v_mov_b32_e32 v83, v0
	v_mov_b32_e32 v84, v0
	v_mov_b32_e32 v85, v0
	v_mov_b32_e32 v86, v0
	v_mov_b32_e32 v87, v0
	v_mov_b32_e32 v96, v0
	s_waitcnt vmcnt(0)
	v_mov_b32_e32 v97, v0
	v_mov_b32_e32 v98, v0
	v_mov_b32_e32 v99, v0
	v_mov_b32_e32 v100, v0
	v_mov_b32_e32 v101, v0
	v_mov_b32_e32 v102, v0
	v_mov_b32_e32 v103, v0
	v_mov_b32_e32 v112, v0
	v_mov_b32_e32 v113, v0
	v_mov_b32_e32 v114, v0
	v_mov_b32_e32 v115, v0
	v_mov_b32_e32 v116, v0
	v_mov_b32_e32 v117, v0
	v_mov_b32_e32 v118, v0
	v_mov_b32_e32 v119, v0
	v_mov_b32_e32 v130, v0
	v_mov_b32_e32 v131, v0
	v_mov_b32_e32 v132, v0
	v_mov_b32_e32 v133, v0
	v_mov_b32_e32 v134, v0
	v_mov_b32_e32 v135, v0
	v_mov_b32_e32 v136, v0
	v_mov_b32_e32 v137, v0
	v_mov_b32_e32 v88, v0
	v_mov_b32_e32 v89, v0
	v_mov_b32_e32 v90, v0
	v_mov_b32_e32 v91, v0
	v_mov_b32_e32 v92, v0
	v_mov_b32_e32 v93, v0
	v_mov_b32_e32 v94, v0
	v_mov_b32_e32 v95, v0
	v_mov_b32_e32 v104, v0
	v_mov_b32_e32 v105, v0
	v_mov_b32_e32 v106, v0
	v_mov_b32_e32 v107, v0
	v_mov_b32_e32 v108, v0
	v_mov_b32_e32 v109, v0
	v_mov_b32_e32 v110, v0
	v_mov_b32_e32 v111, v0
	v_mov_b32_e32 v120, v0
	v_mov_b32_e32 v121, v0
	v_mov_b32_e32 v122, v0
	v_mov_b32_e32 v123, v0
	v_mov_b32_e32 v124, v0
	v_mov_b32_e32 v125, v0
	v_mov_b32_e32 v126, v0
	v_mov_b32_e32 v127, v0
	v_mov_b32_e32 v138, v0
	v_mov_b32_e32 v139, v0
	v_mov_b32_e32 v140, v0
	v_mov_b32_e32 v141, v0
	v_mov_b32_e32 v142, v0
	v_mov_b32_e32 v143, v0
	v_mov_b32_e32 v144, v0
	v_mov_b32_e32 v145, v0
	v_add_u32_e32 v166, 0x10000, v171
.LBB0_342:
	s_add_u32 s12, s10, 0x4000
	s_addc_u32 s13, s11, 0
	s_cmp_eq_u32 s81, 28
	s_cselect_b32 s54, s43, s12
	s_cselect_b32 s55, s9, s13
	s_cselect_b32 s52, s47, s79
	s_cselect_b32 s53, s45, s80
	s_add_u32 s12, s54, 0x8000
	s_addc_u32 s13, s55, 0
	s_add_i32 s82, 0, 0x10000
	s_add_i32 s84, 0, 0x14000
	ds_read_b128 v[48:51], v166
	ds_read_b128 v[52:55], v166 offset:1024
	ds_read_b128 v[64:67], v166 offset:2048
	ds_read_b128 v[68:71], v166 offset:3072
	ds_read_b128 v[146:149], v166 offset:16384
	ds_read_b128 v[150:153], v166 offset:17408
	ds_read_b128 v[180:183], v166 offset:18432
	ds_read_b128 v[184:187], v166 offset:19456
	s_add_i32 m0, s62, 0xc000
	ds_read_b128 v[188:191], v210
	ds_read_b128 v[192:195], v210 offset:1024
	ds_read_b128 v[196:199], v210 offset:2048
	ds_read_b128 v[200:203], v210 offset:3072
	ds_read_b128 v[204:207], v210 offset:4096
	ds_read_b128 v[212:215], v210 offset:5120
	ds_read_b128 v[216:219], v210 offset:6144
	ds_read_b128 v[220:223], v210 offset:7168
	global_load_lds_dwordx4 v176, s[10:11]
	s_add_i32 m0, s62, 0xe000
	s_nop 0
	global_load_lds_dwordx4 v178, s[10:11]
	s_waitcnt vmcnt(8)
	s_waitcnt lgkmcnt(0)
	s_setprio 1
	s_barrier
; #define PG8_STAGE(bufoff, gbase, voff) do { _Pragma("unroll") for (int _i = 0; _i < 2; ++_i) \
;         __builtin_amdgcn_global_load_lds((const unsigned*)((const char*)(gbase) + (voff)[_i]), (PG8_LAS unsigned*)(lds + (bufoff) + ldsw + _i * 8192), 16, 0, 0); } while (0)
; #define PG8_LDA(dst, b, h) do { _Pragma("unroll") for (int m = 0; m < 4; ++m) _Pragma("unroll") for (int k = 0; k < 2; ++k) dst[m][k] = *(const PG8_LAS bf16x8*)(lds + PG8_SA(b, h) + aoff + m * 2048 + k * 1024); } while (0)
; #define PG8_MMA(ai, bj, At, Bt) do { __builtin_amdgcn_s_setprio(1); _Pragma("unroll") for (int m = 0; m < 4; ++m) _Pragma("unroll") for (int n = 0; n < 2; ++n) _Pragma("unroll") for (int k = 0; k < 2; ++k) \
;         acc[ai][bj][m][n] = __builtin_amdgcn_mfma_f32_16x16x32_bf16(Bt[n][k], At[m][k], acc[ai][bj][m][n], 0, 0, 0); __builtin_amdgcn_s_setprio(0); } while (0)
; #define PG8_WAIT_V(n) asm volatile("s_waitcnt vmcnt(" #n ")" ::: "memory")
; #define PG8_WAIT_L(n) asm volatile("s_waitcnt lgkmcnt(" #n ")" ::: "memory")
; #define PG8_BAR __builtin_amdgcn_s_barrier()
; #define PG8_SCHED __builtin_amdgcn_sched_barrier(0)
; template <class Epi, class Sched, bool ALIGN_EPI>
; __device__ __forceinline__ void gemm_phase(PG8_LAS unsigned char* lds, const Gemm g, const Sched& S, const Epi& E, const int tid) {
;     ...
;             PG8_WAIT_V(8); PG8_WAIT_L(0); PG8_BAR; PG8_MMA(0, 0, At, B0); PG8_MMA(0, 1, At, B1); PG8_BAR; PG8_SCHED;
;             PG8_LDA(At, 0, 1); PG8_STAGE(PG8_SB(0, 0), b2, voffB); PG8_STAGE(PG8_SB(0, 1), b2 + hstepB, voffB); PG8_STAGE(PG8_SA(0, 0), a2, voffA);
;             PG8_WAIT_V(8); PG8_WAIT_L(0); PG8_BAR; PG8_MMA(1, 0, At, B0); PG8_MMA(1, 1, At, B1); PG8_BAR; PG8_SCHED;
	v_mfma_f32_16x16x32_bf16 v[142:145], v[48:51], v[188:191], v[142:145]
	v_mfma_f32_16x16x32_bf16 v[138:141], v[64:67], v[188:191], v[138:141]
	v_mfma_f32_16x16x32_bf16 v[124:127], v[48:51], v[196:199], v[124:127]
	v_mfma_f32_16x16x32_bf16 v[120:123], v[64:67], v[196:199], v[120:123]
	v_mfma_f32_16x16x32_bf16 v[108:111], v[48:51], v[204:207], v[108:111]
	v_mfma_f32_16x16x32_bf16 v[104:107], v[64:67], v[204:207], v[104:107]
	v_mfma_f32_16x16x32_bf16 v[92:95], v[48:51], v[216:219], v[92:95]
	v_mfma_f32_16x16x32_bf16 v[88:91], v[64:67], v[216:219], v[88:91]
	v_mfma_f32_16x16x32_bf16 v[142:145], v[52:55], v[192:195], v[142:145]
	v_mfma_f32_16x16x32_bf16 v[138:141], v[68:71], v[192:195], v[138:141]
	v_mfma_f32_16x16x32_bf16 v[124:127], v[52:55], v[200:203], v[124:127]
	v_mfma_f32_16x16x32_bf16 v[120:123], v[68:71], v[200:203], v[120:123]
	v_mfma_f32_16x16x32_bf16 v[108:111], v[52:55], v[212:215], v[108:111]
	v_mfma_f32_16x16x32_bf16 v[104:107], v[68:71], v[212:215], v[104:107]
	v_mfma_f32_16x16x32_bf16 v[92:95], v[52:55], v[220:223], v[92:95]
	v_mfma_f32_16x16x32_bf16 v[88:91], v[68:71], v[220:223], v[88:91]
	v_mfma_f32_16x16x32_bf16 v[134:137], v[146:149], v[188:191], v[134:137]
	v_mfma_f32_16x16x32_bf16 v[130:133], v[180:183], v[188:191], v[130:133]
	v_mfma_f32_16x16x32_bf16 v[116:119], v[146:149], v[196:199], v[116:119]
	v_mfma_f32_16x16x32_bf16 v[112:115], v[180:183], v[196:199], v[112:115]
	v_mfma_f32_16x16x32_bf16 v[100:103], v[146:149], v[204:207], v[100:103]
	v_mfma_f32_16x16x32_bf16 v[96:99], v[180:183], v[204:207], v[96:99]
	v_mfma_f32_16x16x32_bf16 v[84:87], v[146:149], v[216:219], v[84:87]
	v_mfma_f32_16x16x32_bf16 v[80:83], v[180:183], v[216:219], v[80:83]
	v_mfma_f32_16x16x32_bf16 v[134:137], v[150:153], v[192:195], v[134:137]
	v_mfma_f32_16x16x32_bf16 v[130:133], v[184:187], v[192:195], v[130:133]
	v_mfma_f32_16x16x32_bf16 v[116:119], v[150:153], v[200:203], v[116:119]
	v_mfma_f32_16x16x32_bf16 v[112:115], v[184:187], v[200:203], v[112:115]
	v_mfma_f32_16x16x32_bf16 v[100:103], v[150:153], v[212:215], v[100:103]
	v_mfma_f32_16x16x32_bf16 v[96:99], v[184:187], v[212:215], v[96:99]
	v_mfma_f32_16x16x32_bf16 v[84:87], v[150:153], v[220:223], v[84:87]
	v_mfma_f32_16x16x32_bf16 v[80:83], v[184:187], v[220:223], v[80:83]
	s_barrier
	s_setprio 0
	s_add_i32 s82, s82, s59
	s_mov_b32 m0, s82
	ds_read_b128 v[188:191], v210 offset:16384
	ds_read_b128 v[192:195], v210 offset:17408
	ds_read_b128 v[196:199], v210 offset:18432
	ds_read_b128 v[200:203], v210 offset:19456
	ds_read_b128 v[204:207], v210 offset:20480
	ds_read_b128 v[212:215], v210 offset:21504
	ds_read_b128 v[216:219], v210 offset:22528
	ds_read_b128 v[220:223], v210 offset:23552
	global_load_lds_dwordx4 v156, s[52:53]
	s_add_i32 m0, s82, 0x2000
	s_add_u32 s82, s52, 0x4000
	s_addc_u32 s83, s53, 0
	s_add_i32 s84, s84, s59
	global_load_lds_dwordx4 v160, s[52:53]
	s_mov_b32 m0, s84
	s_nop 0
	global_load_lds_dwordx4 v156, s[82:83]
	s_add_i32 m0, s84, 0x2000
	s_nop 0
	global_load_lds_dwordx4 v160, s[82:83]
	s_mov_b32 m0, s62
	s_nop 0
	global_load_lds_dwordx4 v154, s[54:55]
	s_mov_b32 m0, s63
	s_nop 0
	global_load_lds_dwordx4 v158, s[54:55]
	s_waitcnt vmcnt(8)
	s_waitcnt lgkmcnt(0)
	s_setprio 1
	s_barrier
	v_mfma_f32_16x16x32_bf16 v[76:79], v[48:51], v[188:191], v[76:79]
	v_mfma_f32_16x16x32_bf16 v[72:75], v[64:67], v[188:191], v[72:75]
	v_mfma_f32_16x16x32_bf16 v[44:47], v[48:51], v[196:199], v[44:47]
	v_mfma_f32_16x16x32_bf16 v[40:43], v[64:67], v[196:199], v[40:43]
	v_mfma_f32_16x16x32_bf16 v[28:31], v[48:51], v[204:207], v[28:31]
	v_mfma_f32_16x16x32_bf16 v[24:27], v[64:67], v[204:207], v[24:27]
	v_mfma_f32_16x16x32_bf16 v[12:15], v[48:51], v[216:219], v[12:15]
	v_mfma_f32_16x16x32_bf16 v[8:11], v[64:67], v[216:219], v[8:11]
	v_mfma_f32_16x16x32_bf16 v[76:79], v[52:55], v[192:195], v[76:79]
	v_mfma_f32_16x16x32_bf16 v[72:75], v[68:71], v[192:195], v[72:75]
	v_mfma_f32_16x16x32_bf16 v[44:47], v[52:55], v[200:203], v[44:47]
	v_mfma_f32_16x16x32_bf16 v[40:43], v[68:71], v[200:203], v[40:43]
	v_mfma_f32_16x16x32_bf16 v[28:31], v[52:55], v[212:215], v[28:31]
	v_mfma_f32_16x16x32_bf16 v[24:27], v[68:71], v[212:215], v[24:27]
	v_mfma_f32_16x16x32_bf16 v[12:15], v[52:55], v[220:223], v[12:15]
	v_mfma_f32_16x16x32_bf16 v[8:11], v[68:71], v[220:223], v[8:11]
	v_mfma_f32_16x16x32_bf16 v[36:39], v[146:149], v[196:199], v[36:39]
	v_mfma_f32_16x16x32_bf16 v[32:35], v[180:183], v[196:199], v[32:35]
	v_mfma_f32_16x16x32_bf16 v[20:23], v[146:149], v[204:207], v[20:23]
	v_mfma_f32_16x16x32_bf16 v[16:19], v[180:183], v[204:207], v[16:19]
	v_mfma_f32_16x16x32_bf16 v[4:7], v[146:149], v[216:219], v[4:7]
	v_mfma_f32_16x16x32_bf16 v[0:3], v[180:183], v[216:219], v[0:3]
	v_mfma_f32_16x16x32_bf16 v[48:51], v[146:149], v[188:191], v[60:63]
	v_mfma_f32_16x16x32_bf16 v[52:55], v[180:183], v[188:191], v[56:59]
	v_mfma_f32_16x16x32_bf16 v[36:39], v[150:153], v[200:203], v[36:39]
	v_mfma_f32_16x16x32_bf16 v[32:35], v[184:187], v[200:203], v[32:35]
	v_mfma_f32_16x16x32_bf16 v[20:23], v[150:153], v[212:215], v[20:23]
	v_mfma_f32_16x16x32_bf16 v[16:19], v[184:187], v[212:215], v[16:19]
	v_mfma_f32_16x16x32_bf16 v[4:7], v[150:153], v[220:223], v[4:7]
	v_mfma_f32_16x16x32_bf16 v[0:3], v[184:187], v[220:223], v[0:3]
	v_mfma_f32_16x16x32_bf16 v[48:51], v[150:153], v[192:195], v[48:51]
	v_mfma_f32_16x16x32_bf16 v[52:55], v[184:187], v[192:195], v[52:55]
	s_barrier
; #define PG8_STAGE(bufoff, gbase, voff) do { _Pragma("unroll") for (int _i = 0; _i < 2; ++_i) \
;         __builtin_amdgcn_global_load_lds((const unsigned*)((const char*)(gbase) + (voff)[_i]), (PG8_LAS unsigned*)(lds + (bufoff) + ldsw + _i * 8192), 16, 0, 0); } while (0)
; #define PG8_LDA(dst, b, h) do { _Pragma("unroll") for (int m = 0; m < 4; ++m) _Pragma("unroll") for (int k = 0; k < 2; ++k) dst[m][k] = *(const PG8_LAS bf16x8*)(lds + PG8_SA(b, h) + aoff + m * 2048 + k * 1024); } while (0)
; #define PG8_LDB(dst, b, h) do { _Pragma("unroll") for (int n = 0; n < 2; ++n) _Pragma("unroll") for (int k = 0; k < 2; ++k) dst[n][k] = *(const PG8_LAS bf16x8*)(lds + PG8_SB(b, h) + boff + n * 2048 + k * 1024); } while (0)
; #define PG8_MMA(ai, bj, At, Bt) do { __builtin_amdgcn_s_setprio(1); _Pragma("unroll") for (int m = 0; m < 4; ++m) _Pragma("unroll") for (int n = 0; n < 2; ++n) _Pragma("unroll") for (int k = 0; k < 2; ++k) \
;         acc[ai][bj][m][n] = __builtin_amdgcn_mfma_f32_16x16x32_bf16(Bt[n][k], At[m][k], acc[ai][bj][m][n], 0, 0, 0); __builtin_amdgcn_s_setprio(0); } while (0)
; #define PG8_WAIT_V(n) asm volatile("s_waitcnt vmcnt(" #n ")" ::: "memory")
; #define PG8_WAIT_L(n) asm volatile("s_waitcnt lgkmcnt(" #n ")" ::: "memory")
; #define PG8_BAR __builtin_amdgcn_s_barrier()
; #define PG8_SCHED __builtin_amdgcn_sched_barrier(0)
; template <class Epi, class Sched, bool ALIGN_EPI>
; __device__ __forceinline__ void gemm_phase(PG8_LAS unsigned char* lds, const Gemm g, const Sched& S, const Epi& E, const int tid) {
;     ...
;             PG8_LDB(B0, 1, 0); PG8_LDB(B1, 1, 1); PG8_SCHED; PG8_LDA(At, 1, 0); PG8_STAGE(PG8_SA(0, 1), a2 + hstepA, voffA);
;             PG8_WAIT_V(8); PG8_WAIT_L(0); PG8_BAR; PG8_MMA(0, 0, At, B0); PG8_MMA(0, 1, At, B1); PG8_BAR; PG8_SCHED;
;             PG8_LDA(At, 1, 1); PG8_STAGE(PG8_SB(1, 0), b3, voffB); PG8_STAGE(PG8_SB(1, 1), b3 + hstepB, voffB); PG8_STAGE(PG8_SA(1, 0), a3, voffA);
;             PG8_WAIT_V(8); PG8_WAIT_L(0); PG8_BAR; PG8_MMA(1, 0, At, B0); PG8_MMA(1, 1, At, B1); PG8_BAR; PG8_SCHED;
;         }
	s_setprio 0
	s_add_i32 s82, 0, 0x18000
	s_add_i32 s83, 0, 0x1c000
	ds_read_b128 v[56:59], v166 offset:32768
	ds_read_b128 v[60:63], v166 offset:33792
	ds_read_b128 v[64:67], v166 offset:34816
	ds_read_b128 v[68:71], v166 offset:35840
	ds_read_b128 v[146:149], v166 offset:49152
	ds_read_b128 v[150:153], v166 offset:50176
	ds_read_b128 v[180:183], v166 offset:51200
	ds_read_b128 v[184:187], v166 offset:52224
	s_add_u32 s54, s54, 0x4000
	s_addc_u32 s55, s55, 0
	s_mov_b32 m0, s64
	ds_read_b128 v[188:191], v210 offset:32768
	ds_read_b128 v[192:195], v210 offset:33792
	ds_read_b128 v[196:199], v210 offset:34816
	ds_read_b128 v[200:203], v210 offset:35840
	ds_read_b128 v[204:207], v210 offset:36864
	ds_read_b128 v[212:215], v210 offset:37888
	ds_read_b128 v[216:219], v210 offset:38912
	ds_read_b128 v[220:223], v210 offset:39936
	global_load_lds_dwordx4 v154, s[54:55]
	s_mov_b32 m0, s65
	s_nop 0
	global_load_lds_dwordx4 v158, s[54:55]
	s_waitcnt vmcnt(8)
	s_waitcnt lgkmcnt(0)
	s_setprio 1
	s_barrier
	v_mfma_f32_16x16x32_bf16 v[142:145], v[56:59], v[188:191], v[142:145]
	v_mfma_f32_16x16x32_bf16 v[138:141], v[64:67], v[188:191], v[138:141]
	v_mfma_f32_16x16x32_bf16 v[124:127], v[56:59], v[196:199], v[124:127]
	v_mfma_f32_16x16x32_bf16 v[120:123], v[64:67], v[196:199], v[120:123]
	v_mfma_f32_16x16x32_bf16 v[108:111], v[56:59], v[204:207], v[108:111]
	v_mfma_f32_16x16x32_bf16 v[104:107], v[64:67], v[204:207], v[104:107]
	v_mfma_f32_16x16x32_bf16 v[92:95], v[56:59], v[216:219], v[92:95]
	v_mfma_f32_16x16x32_bf16 v[88:91], v[64:67], v[216:219], v[88:91]
	v_mfma_f32_16x16x32_bf16 v[142:145], v[60:63], v[192:195], v[142:145]
	v_mfma_f32_16x16x32_bf16 v[138:141], v[68:71], v[192:195], v[138:141]
	v_mfma_f32_16x16x32_bf16 v[124:127], v[60:63], v[200:203], v[124:127]
	v_mfma_f32_16x16x32_bf16 v[120:123], v[68:71], v[200:203], v[120:123]
	v_mfma_f32_16x16x32_bf16 v[108:111], v[60:63], v[212:215], v[108:111]
	v_mfma_f32_16x16x32_bf16 v[104:107], v[68:71], v[212:215], v[104:107]
	v_mfma_f32_16x16x32_bf16 v[92:95], v[60:63], v[220:223], v[92:95]
	v_mfma_f32_16x16x32_bf16 v[88:91], v[68:71], v[220:223], v[88:91]
	v_mfma_f32_16x16x32_bf16 v[134:137], v[146:149], v[188:191], v[134:137]
	v_mfma_f32_16x16x32_bf16 v[130:133], v[180:183], v[188:191], v[130:133]
	v_mfma_f32_16x16x32_bf16 v[116:119], v[146:149], v[196:199], v[116:119]
	v_mfma_f32_16x16x32_bf16 v[112:115], v[180:183], v[196:199], v[112:115]
	v_mfma_f32_16x16x32_bf16 v[100:103], v[146:149], v[204:207], v[100:103]
	v_mfma_f32_16x16x32_bf16 v[96:99], v[180:183], v[204:207], v[96:99]
	v_mfma_f32_16x16x32_bf16 v[84:87], v[146:149], v[216:219], v[84:87]
	v_mfma_f32_16x16x32_bf16 v[80:83], v[180:183], v[216:219], v[80:83]
	v_mfma_f32_16x16x32_bf16 v[134:137], v[150:153], v[192:195], v[134:137]
	v_mfma_f32_16x16x32_bf16 v[130:133], v[184:187], v[192:195], v[130:133]
	v_mfma_f32_16x16x32_bf16 v[116:119], v[150:153], v[200:203], v[116:119]
	v_mfma_f32_16x16x32_bf16 v[112:115], v[184:187], v[200:203], v[112:115]
	v_mfma_f32_16x16x32_bf16 v[100:103], v[150:153], v[212:215], v[100:103]
	v_mfma_f32_16x16x32_bf16 v[96:99], v[184:187], v[212:215], v[96:99]
	v_mfma_f32_16x16x32_bf16 v[84:87], v[150:153], v[220:223], v[84:87]
	v_mfma_f32_16x16x32_bf16 v[80:83], v[184:187], v[220:223], v[80:83]
	s_barrier
	s_setprio 0
	s_add_u32 s54, s52, 0x8000
	s_addc_u32 s55, s53, 0
	s_add_i32 s82, s82, s59
	s_mov_b32 m0, s82
	ds_read_b128 v[188:191], v210 offset:49152
	ds_read_b128 v[192:195], v210 offset:50176
	ds_read_b128 v[196:199], v210 offset:51200
	ds_read_b128 v[200:203], v210 offset:52224
	ds_read_b128 v[204:207], v210 offset:53248
	ds_read_b128 v[212:215], v210 offset:54272
	ds_read_b128 v[216:219], v210 offset:55296
	ds_read_b128 v[220:223], v210 offset:56320
	global_load_lds_dwordx4 v156, s[54:55]
	s_add_i32 m0, s82, 0x2000
	s_add_u32 s52, s52, 0xc000
	s_addc_u32 s53, s53, 0
	global_load_lds_dwordx4 v160, s[54:55]
	s_add_i32 s54, s83, s59
	s_mov_b32 m0, s54
	s_nop 0
	global_load_lds_dwordx4 v156, s[52:53]
	s_add_i32 m0, s54, 0x2000
	s_nop 0
	global_load_lds_dwordx4 v160, s[52:53]
	s_mov_b32 m0, s66
	s_nop 0
	global_load_lds_dwordx4 v154, s[12:13]
	s_mov_b32 m0, s67
	s_nop 0
	global_load_lds_dwordx4 v158, s[12:13]
	s_waitcnt vmcnt(8)
	s_waitcnt lgkmcnt(0)
	s_setprio 1
	s_barrier
	v_mfma_f32_16x16x32_bf16 v[76:79], v[56:59], v[188:191], v[76:79]
	v_mfma_f32_16x16x32_bf16 v[72:75], v[64:67], v[188:191], v[72:75]
	v_mfma_f32_16x16x32_bf16 v[44:47], v[56:59], v[196:199], v[44:47]
	v_mfma_f32_16x16x32_bf16 v[40:43], v[64:67], v[196:199], v[40:43]
	v_mfma_f32_16x16x32_bf16 v[28:31], v[56:59], v[204:207], v[28:31]
	v_mfma_f32_16x16x32_bf16 v[24:27], v[64:67], v[204:207], v[24:27]
	v_mfma_f32_16x16x32_bf16 v[12:15], v[56:59], v[216:219], v[12:15]
	v_mfma_f32_16x16x32_bf16 v[8:11], v[64:67], v[216:219], v[8:11]
	v_mfma_f32_16x16x32_bf16 v[76:79], v[60:63], v[192:195], v[76:79]
	v_mfma_f32_16x16x32_bf16 v[72:75], v[68:71], v[192:195], v[72:75]
	v_mfma_f32_16x16x32_bf16 v[44:47], v[60:63], v[200:203], v[44:47]
	v_mfma_f32_16x16x32_bf16 v[40:43], v[68:71], v[200:203], v[40:43]
	v_mfma_f32_16x16x32_bf16 v[28:31], v[60:63], v[212:215], v[28:31]
	v_mfma_f32_16x16x32_bf16 v[24:27], v[68:71], v[212:215], v[24:27]
	v_mfma_f32_16x16x32_bf16 v[12:15], v[60:63], v[220:223], v[12:15]
	v_mfma_f32_16x16x32_bf16 v[8:11], v[68:71], v[220:223], v[8:11]
	v_mfma_f32_16x16x32_bf16 v[48:51], v[146:149], v[188:191], v[48:51]
	v_mfma_f32_16x16x32_bf16 v[60:63], v[150:153], v[192:195], v[48:51]
	v_mfma_f32_16x16x32_bf16 v[48:51], v[180:183], v[188:191], v[52:55]
	v_mfma_f32_16x16x32_bf16 v[36:39], v[146:149], v[196:199], v[36:39]
	v_mfma_f32_16x16x32_bf16 v[32:35], v[180:183], v[196:199], v[32:35]
	v_mfma_f32_16x16x32_bf16 v[20:23], v[146:149], v[204:207], v[20:23]
	v_mfma_f32_16x16x32_bf16 v[16:19], v[180:183], v[204:207], v[16:19]
	v_mfma_f32_16x16x32_bf16 v[4:7], v[146:149], v[216:219], v[4:7]
	v_mfma_f32_16x16x32_bf16 v[0:3], v[180:183], v[216:219], v[0:3]
	v_mfma_f32_16x16x32_bf16 v[56:59], v[184:187], v[192:195], v[48:51]
	v_mfma_f32_16x16x32_bf16 v[36:39], v[150:153], v[200:203], v[36:39]
	v_mfma_f32_16x16x32_bf16 v[32:35], v[184:187], v[200:203], v[32:35]
	v_mfma_f32_16x16x32_bf16 v[20:23], v[150:153], v[212:215], v[20:23]
	v_mfma_f32_16x16x32_bf16 v[16:19], v[184:187], v[212:215], v[16:19]
	v_mfma_f32_16x16x32_bf16 v[4:7], v[150:153], v[220:223], v[4:7]
	v_mfma_f32_16x16x32_bf16 v[0:3], v[184:187], v[220:223], v[0:3]
	s_barrier
	s_setprio 0
	s_add_i32 s81, s81, 2
	s_add_u32 s10, s10, 0x10000
	s_addc_u32 s11, s11, 0
	s_add_u32 s79, s79, 0x10000
	s_addc_u32 s80, s80, 0
	s_cmp_gt_u32 s81, 29
	s_cbranch_scc0 .LBB0_342
	s_and_b64 vcc, exec, s[34:35]
	s_cbranch_vccz .LBB0_345
	s_barrier

; #define PG8_STAGE(bufoff, gbase, voff) do { _Pragma("unroll") for (int _i = 0; _i < 2; ++_i) \
;         __builtin_amdgcn_global_load_lds((const unsigned*)((const char*)(gbase) + (voff)[_i]), (PG8_LAS unsigned*)(lds + (bufoff) + ldsw + _i * 8192), 16, 0, 0); } while (0)
; #define PG8_LDA(dst, b, h) do { _Pragma("unroll") for (int m = 0; m < 4; ++m) _Pragma("unroll") for (int k = 0; k < 2; ++k) dst[m][k] = *(const PG8_LAS bf16x8*)(lds + PG8_SA(b, h) + aoff + m * 2048 + k * 1024); } while (0)
; #define PG8_LDB(dst, b, h) do { _Pragma("unroll") for (int n = 0; n < 2; ++n) _Pragma("unroll") for (int k = 0; k < 2; ++k) dst[n][k] = *(const PG8_LAS bf16x8*)(lds + PG8_SB(b, h) + boff + n * 2048 + k * 1024); } while (0)
; #define PG8_MMA(ai, bj, At, Bt) do { __builtin_amdgcn_s_setprio(1); _Pragma("unroll") for (int m = 0; m < 4; ++m) _Pragma("unroll") for (int n = 0; n < 2; ++n) _Pragma("unroll") for (int k = 0; k < 2; ++k) \
;         acc[ai][bj][m][n] = __builtin_amdgcn_mfma_f32_16x16x32_bf16(Bt[n][k], At[m][k], acc[ai][bj][m][n], 0, 0, 0); __builtin_amdgcn_s_setprio(0); } while (0)
; #define PG8_WAIT_V(n) asm volatile("s_waitcnt vmcnt(" #n ")" ::: "memory")
; #define PG8_WAIT_L(n) asm volatile("s_waitcnt lgkmcnt(" #n ")" ::: "memory")
; #define PG8_BAR __builtin_amdgcn_s_barrier()
; template <class Epi, class Sched, bool ALIGN_EPI>
; __device__ __forceinline__ void gemm_phase(PG8_LAS unsigned char* lds, const Gemm g, const Sched& S, const Epi& E, const int tid) {
;     ...
;             const bool last = (t == nt - 2);
;             const char* a1 = cA + (size_t)(t + 1) * kstepA;
;             const char* a2 = last ? nA : cA + (size_t)(t + 2) * kstepA; const char* b2 = last ? nB : cB + (size_t)(t + 2) * kstepB;
;             const char* a3 = a2 + kstepA; const char* b3 = b2 + kstepB;
;             if (last && has_next) S.a_ready(nxt);
;             PG8_LDB(B0, 0, 0); PG8_LDB(B1, 0, 1); PG8_SCHED; PG8_LDA(At, 0, 0); PG8_STAGE(PG8_SA(1, 1), a1 + hstepA, voffA);
;             PG8_WAIT_V(8); PG8_WAIT_L(0); PG8_BAR; PG8_MMA(0, 0, At, B0); PG8_MMA(0, 1, At, B1); PG8_BAR; PG8_SCHED;
;             PG8_LDA(At, 0, 1); PG8_STAGE(PG8_SB(0, 0), b2, voffB); PG8_STAGE(PG8_SB(0, 1), b2 + hstepB, voffB); PG8_STAGE(PG8_SA(0, 0), a2, voffA);
;             PG8_WAIT_V(8); PG8_WAIT_L(0); PG8_BAR; PG8_MMA(1, 0, At, B0); PG8_MMA(1, 1, At, B1); PG8_BAR; PG8_SCHED;
.LBB0_1396:
	s_add_u32 s54, s20, 1
	s_addc_u32 s55, s21, 0
	s_add_u32 s22, s20, 2
	s_addc_u32 s23, s21, 0
	s_lshl_b64 s[24:25], s[22:23], s44
	s_add_u32 s21, s18, s24
	s_addc_u32 s24, s19, s25
	s_cmp_eq_u32 s45, s20
	s_cselect_b32 s26, s8, s21
	s_cselect_b32 s27, s9, s24
	s_cselect_b32 s24, s16, s52
	s_cselect_b32 s25, s17, s53
	s_add_u32 s20, s26, s38
	s_addc_u32 s21, s27, 0
	s_add_i32 s56, 0, 0x10000
	s_add_i32 s57, 0, 0x14000
	v_add_u32_e32 v108, s56, v195
	v_add_u32_e32 v128, s57, v195
	ds_read_b128 v[88:91], v108
	ds_read_b128 v[92:95], v108 offset:1024
	ds_read_b128 v[100:103], v108 offset:2048
	ds_read_b128 v[108:111], v108 offset:3072
	ds_read_b128 v[146:149], v128
	ds_read_b128 v[150:153], v128 offset:1024
	ds_read_b128 v[154:157], v128 offset:2048
	ds_read_b128 v[158:161], v128 offset:3072
	s_lshl_b64 s[54:55], s[54:55], s44
	s_add_u32 s54, s50, s54
	s_addc_u32 s55, s51, s55
	v_lshl_add_u64 v[192:193], s[54:55], 0, v[176:177]
	s_add_i32 m0, s31, 0xc000
	ds_read_b128 v[162:165], v185
	ds_read_b128 v[166:169], v185 offset:1024
	ds_read_b128 v[172:175], v185 offset:2048
	ds_read_b128 v[188:191], v185 offset:3072
	ds_read_b128 v[196:199], v185 offset:4096
	ds_read_b128 v[200:203], v185 offset:5120
	ds_read_b128 v[204:207], v185 offset:6144
	ds_read_b128 v[208:211], v185 offset:7168
	global_load_lds_dwordx4 v[192:193], off
	v_lshl_add_u64 v[192:193], s[54:55], 0, v[180:181]
	s_add_i32 m0, s31, 0xe000
	s_nop 0
	global_load_lds_dwordx4 v[192:193], off
	s_waitcnt vmcnt(8)
	s_waitcnt lgkmcnt(0)
	s_setprio 1
	s_barrier
	v_mfma_f32_16x16x32_bf16 v[142:145], v[88:91], v[162:165], v[142:145]
	v_mfma_f32_16x16x32_bf16 v[138:141], v[100:103], v[162:165], v[138:141]
	v_mfma_f32_16x16x32_bf16 v[124:127], v[88:91], v[172:175], v[124:127]
	v_mfma_f32_16x16x32_bf16 v[120:123], v[100:103], v[172:175], v[120:123]
	v_mfma_f32_16x16x32_bf16 v[104:107], v[88:91], v[196:199], v[104:107]
	v_mfma_f32_16x16x32_bf16 v[96:99], v[100:103], v[196:199], v[96:99]
	v_mfma_f32_16x16x32_bf16 v[76:79], v[88:91], v[204:207], v[76:79]
	v_mfma_f32_16x16x32_bf16 v[72:75], v[100:103], v[204:207], v[72:75]
	v_mfma_f32_16x16x32_bf16 v[142:145], v[92:95], v[166:169], v[142:145]
	v_mfma_f32_16x16x32_bf16 v[138:141], v[108:111], v[166:169], v[138:141]
	v_mfma_f32_16x16x32_bf16 v[124:127], v[92:95], v[188:191], v[124:127]
	v_mfma_f32_16x16x32_bf16 v[120:123], v[108:111], v[188:191], v[120:123]
	v_mfma_f32_16x16x32_bf16 v[104:107], v[92:95], v[200:203], v[104:107]
	v_mfma_f32_16x16x32_bf16 v[96:99], v[108:111], v[200:203], v[96:99]
	v_mfma_f32_16x16x32_bf16 v[76:79], v[92:95], v[208:211], v[76:79]
	v_mfma_f32_16x16x32_bf16 v[72:75], v[108:111], v[208:211], v[72:75]
	v_mfma_f32_16x16x32_bf16 v[134:137], v[146:149], v[162:165], v[134:137]
	v_mfma_f32_16x16x32_bf16 v[130:133], v[154:157], v[162:165], v[130:133]
	v_mfma_f32_16x16x32_bf16 v[116:119], v[146:149], v[172:175], v[116:119]
	v_mfma_f32_16x16x32_bf16 v[112:115], v[154:157], v[172:175], v[112:115]
	v_mfma_f32_16x16x32_bf16 v[84:87], v[146:149], v[196:199], v[84:87]
	v_mfma_f32_16x16x32_bf16 v[80:83], v[154:157], v[196:199], v[80:83]
	v_mfma_f32_16x16x32_bf16 v[68:71], v[146:149], v[204:207], v[68:71]
	v_mfma_f32_16x16x32_bf16 v[64:67], v[154:157], v[204:207], v[64:67]
	v_mfma_f32_16x16x32_bf16 v[134:137], v[150:153], v[166:169], v[134:137]
	v_mfma_f32_16x16x32_bf16 v[130:133], v[158:161], v[166:169], v[130:133]
	v_mfma_f32_16x16x32_bf16 v[116:119], v[150:153], v[188:191], v[116:119]
	v_mfma_f32_16x16x32_bf16 v[112:115], v[158:161], v[188:191], v[112:115]
	v_mfma_f32_16x16x32_bf16 v[84:87], v[150:153], v[200:203], v[84:87]
	v_mfma_f32_16x16x32_bf16 v[80:83], v[158:161], v[200:203], v[80:83]
	v_mfma_f32_16x16x32_bf16 v[68:71], v[150:153], v[208:211], v[68:71]
	v_mfma_f32_16x16x32_bf16 v[64:67], v[158:161], v[208:211], v[64:67]
	s_barrier
	s_setprio 0
	s_add_i32 s54, s56, s30
	v_lshl_add_u64 v[192:193], s[24:25], 0, v[178:179]
	s_mov_b32 m0, s54
	ds_read_b128 v[162:165], v185 offset:16384
	ds_read_b128 v[166:169], v185 offset:17408
	ds_read_b128 v[172:175], v185 offset:18432
	ds_read_b128 v[188:191], v185 offset:19456
	ds_read_b128 v[196:199], v185 offset:20480
	ds_read_b128 v[200:203], v185 offset:21504
	ds_read_b128 v[204:207], v185 offset:22528
	ds_read_b128 v[208:211], v185 offset:23552
	global_load_lds_dwordx4 v[192:193], off
	s_add_i32 m0, s54, 0x2000
	s_add_u32 s54, s24, 0x4000
	v_lshl_add_u64 v[192:193], s[24:25], 0, v[182:183]
	s_addc_u32 s55, s25, 0
	s_add_i32 s56, s57, s30
	global_load_lds_dwordx4 v[192:193], off
	v_lshl_add_u64 v[192:193], s[54:55], 0, v[178:179]
	s_mov_b32 m0, s56
	s_nop 0
	global_load_lds_dwordx4 v[192:193], off
	v_lshl_add_u64 v[192:193], s[54:55], 0, v[182:183]
	s_add_i32 m0, s56, 0x2000
	s_nop 0
	global_load_lds_dwordx4 v[192:193], off
	v_lshl_add_u64 v[192:193], s[26:27], 0, v[176:177]
	s_mov_b32 m0, s31
	s_nop 0
	global_load_lds_dwordx4 v[192:193], off
	v_lshl_add_u64 v[192:193], s[26:27], 0, v[180:181]
	s_mov_b32 m0, s33
	s_nop 0
	global_load_lds_dwordx4 v[192:193], off
	s_waitcnt vmcnt(8)
	s_waitcnt lgkmcnt(0)
	s_setprio 1
	s_barrier
; #define PG8_STAGE(bufoff, gbase, voff) do { _Pragma("unroll") for (int _i = 0; _i < 2; ++_i) \
;         __builtin_amdgcn_global_load_lds((const unsigned*)((const char*)(gbase) + (voff)[_i]), (PG8_LAS unsigned*)(lds + (bufoff) + ldsw + _i * 8192), 16, 0, 0); } while (0)
; #define PG8_LDA(dst, b, h) do { _Pragma("unroll") for (int m = 0; m < 4; ++m) _Pragma("unroll") for (int k = 0; k < 2; ++k) dst[m][k] = *(const PG8_LAS bf16x8*)(lds + PG8_SA(b, h) + aoff + m * 2048 + k * 1024); } while (0)
; #define PG8_LDB(dst, b, h) do { _Pragma("unroll") for (int n = 0; n < 2; ++n) _Pragma("unroll") for (int k = 0; k < 2; ++k) dst[n][k] = *(const PG8_LAS bf16x8*)(lds + PG8_SB(b, h) + boff + n * 2048 + k * 1024); } while (0)
; #define PG8_MMA(ai, bj, At, Bt) do { __builtin_amdgcn_s_setprio(1); _Pragma("unroll") for (int m = 0; m < 4; ++m) _Pragma("unroll") for (int n = 0; n < 2; ++n) _Pragma("unroll") for (int k = 0; k < 2; ++k) \
;         acc[ai][bj][m][n] = __builtin_amdgcn_mfma_f32_16x16x32_bf16(Bt[n][k], At[m][k], acc[ai][bj][m][n], 0, 0, 0); __builtin_amdgcn_s_setprio(0); } while (0)
; #define PG8_WAIT_V(n) asm volatile("s_waitcnt vmcnt(" #n ")" ::: "memory")
; #define PG8_WAIT_L(n) asm volatile("s_waitcnt lgkmcnt(" #n ")" ::: "memory")
; #define PG8_BAR __builtin_amdgcn_s_barrier()
; #define PG8_SCHED __builtin_amdgcn_sched_barrier(0)
; template <class Epi, class Sched, bool ALIGN_EPI>
; __device__ __forceinline__ void gemm_phase(PG8_LAS unsigned char* lds, const Gemm g, const Sched& S, const Epi& E, const int tid) {
;     ...
;             PG8_WAIT_V(8); PG8_WAIT_L(0); PG8_BAR; PG8_MMA(1, 0, At, B0); PG8_MMA(1, 1, At, B1); PG8_BAR; PG8_SCHED;
;             PG8_LDB(B0, 1, 0); PG8_LDB(B1, 1, 1); PG8_SCHED; PG8_LDA(At, 1, 0); PG8_STAGE(PG8_SA(0, 1), a2 + hstepA, voffA);
;             PG8_WAIT_V(8); PG8_WAIT_L(0); PG8_BAR; PG8_MMA(0, 0, At, B0); PG8_MMA(0, 1, At, B1); PG8_BAR; PG8_SCHED;
	v_mfma_f32_16x16x32_bf16 v[60:63], v[88:91], v[162:165], v[60:63]
	v_mfma_f32_16x16x32_bf16 v[56:59], v[100:103], v[162:165], v[56:59]
	v_mfma_f32_16x16x32_bf16 v[44:47], v[88:91], v[172:175], v[44:47]
	v_mfma_f32_16x16x32_bf16 v[40:43], v[100:103], v[172:175], v[40:43]
	v_mfma_f32_16x16x32_bf16 v[28:31], v[88:91], v[196:199], v[28:31]
	v_mfma_f32_16x16x32_bf16 v[24:27], v[100:103], v[196:199], v[24:27]
	v_mfma_f32_16x16x32_bf16 v[12:15], v[88:91], v[204:207], v[12:15]
	v_mfma_f32_16x16x32_bf16 v[8:11], v[100:103], v[204:207], v[8:11]
	v_mfma_f32_16x16x32_bf16 v[60:63], v[92:95], v[166:169], v[60:63]
	v_mfma_f32_16x16x32_bf16 v[56:59], v[108:111], v[166:169], v[56:59]
	v_mfma_f32_16x16x32_bf16 v[44:47], v[92:95], v[188:191], v[44:47]
	v_mfma_f32_16x16x32_bf16 v[40:43], v[108:111], v[188:191], v[40:43]
	v_mfma_f32_16x16x32_bf16 v[28:31], v[92:95], v[200:203], v[28:31]
	v_mfma_f32_16x16x32_bf16 v[24:27], v[108:111], v[200:203], v[24:27]
	v_mfma_f32_16x16x32_bf16 v[12:15], v[92:95], v[208:211], v[12:15]
	v_mfma_f32_16x16x32_bf16 v[8:11], v[108:111], v[208:211], v[8:11]
	v_mfma_f32_16x16x32_bf16 v[52:55], v[146:149], v[162:165], v[52:55]
	v_mfma_f32_16x16x32_bf16 v[48:51], v[154:157], v[162:165], v[48:51]
	v_mfma_f32_16x16x32_bf16 v[36:39], v[146:149], v[172:175], v[36:39]
	v_mfma_f32_16x16x32_bf16 v[32:35], v[154:157], v[172:175], v[32:35]
	v_mfma_f32_16x16x32_bf16 v[20:23], v[146:149], v[196:199], v[20:23]
	v_mfma_f32_16x16x32_bf16 v[16:19], v[154:157], v[196:199], v[16:19]
	v_mfma_f32_16x16x32_bf16 v[4:7], v[146:149], v[204:207], v[4:7]
	v_mfma_f32_16x16x32_bf16 v[0:3], v[154:157], v[204:207], v[0:3]
	v_mfma_f32_16x16x32_bf16 v[52:55], v[150:153], v[166:169], v[52:55]
	v_mfma_f32_16x16x32_bf16 v[48:51], v[158:161], v[166:169], v[48:51]
	v_mfma_f32_16x16x32_bf16 v[36:39], v[150:153], v[188:191], v[36:39]
	v_mfma_f32_16x16x32_bf16 v[32:35], v[158:161], v[188:191], v[32:35]
	v_mfma_f32_16x16x32_bf16 v[20:23], v[150:153], v[200:203], v[20:23]
	v_mfma_f32_16x16x32_bf16 v[16:19], v[158:161], v[200:203], v[16:19]
	v_mfma_f32_16x16x32_bf16 v[4:7], v[150:153], v[208:211], v[4:7]
	v_mfma_f32_16x16x32_bf16 v[0:3], v[158:161], v[208:211], v[0:3]
	s_barrier
	s_setprio 0
	s_add_i32 s54, 0, 0x18000
	s_add_i32 s55, 0, 0x1c000
	v_add_u32_e32 v108, s54, v195
	v_add_u32_e32 v128, s55, v195
	ds_read_b128 v[88:91], v108
	ds_read_b128 v[92:95], v108 offset:1024
	ds_read_b128 v[100:103], v108 offset:2048
	ds_read_b128 v[108:111], v108 offset:3072
	ds_read_b128 v[146:149], v128
	ds_read_b128 v[150:153], v128 offset:1024
	ds_read_b128 v[154:157], v128 offset:2048
	ds_read_b128 v[158:161], v128 offset:3072
	s_add_u32 s26, s26, s68
	s_addc_u32 s27, s27, s69
	s_mov_b32 m0, s34
	v_lshl_add_u64 v[192:193], s[26:27], 0, v[176:177]
	ds_read_b128 v[162:165], v185 offset:32768
	ds_read_b128 v[166:169], v185 offset:33792
	ds_read_b128 v[172:175], v185 offset:34816
	ds_read_b128 v[188:191], v185 offset:35840
	ds_read_b128 v[196:199], v185 offset:36864
	ds_read_b128 v[200:203], v185 offset:37888
	ds_read_b128 v[204:207], v185 offset:38912
	ds_read_b128 v[208:211], v185 offset:39936
	global_load_lds_dwordx4 v[192:193], off
	v_lshl_add_u64 v[192:193], s[26:27], 0, v[180:181]
	s_mov_b32 m0, s35
	s_nop 0
	global_load_lds_dwordx4 v[192:193], off
	s_waitcnt vmcnt(8)
	s_waitcnt lgkmcnt(0)
	s_setprio 1
	s_barrier
	v_mfma_f32_16x16x32_bf16 v[142:145], v[88:91], v[162:165], v[142:145]
	v_mfma_f32_16x16x32_bf16 v[138:141], v[100:103], v[162:165], v[138:141]
	v_mfma_f32_16x16x32_bf16 v[124:127], v[88:91], v[172:175], v[124:127]
	v_mfma_f32_16x16x32_bf16 v[120:123], v[100:103], v[172:175], v[120:123]
	v_mfma_f32_16x16x32_bf16 v[104:107], v[88:91], v[196:199], v[104:107]
	v_mfma_f32_16x16x32_bf16 v[96:99], v[100:103], v[196:199], v[96:99]
	v_mfma_f32_16x16x32_bf16 v[76:79], v[88:91], v[204:207], v[76:79]
	v_mfma_f32_16x16x32_bf16 v[72:75], v[100:103], v[204:207], v[72:75]
	v_mfma_f32_16x16x32_bf16 v[142:145], v[92:95], v[166:169], v[142:145]
	v_mfma_f32_16x16x32_bf16 v[138:141], v[108:111], v[166:169], v[138:141]
	v_mfma_f32_16x16x32_bf16 v[124:127], v[92:95], v[188:191], v[124:127]
	v_mfma_f32_16x16x32_bf16 v[120:123], v[108:111], v[188:191], v[120:123]
	v_mfma_f32_16x16x32_bf16 v[104:107], v[92:95], v[200:203], v[104:107]
	v_mfma_f32_16x16x32_bf16 v[96:99], v[108:111], v[200:203], v[96:99]
	v_mfma_f32_16x16x32_bf16 v[76:79], v[92:95], v[208:211], v[76:79]
	v_mfma_f32_16x16x32_bf16 v[72:75], v[108:111], v[208:211], v[72:75]
	v_mfma_f32_16x16x32_bf16 v[134:137], v[146:149], v[162:165], v[134:137]
	v_mfma_f32_16x16x32_bf16 v[130:133], v[154:157], v[162:165], v[130:133]
	v_mfma_f32_16x16x32_bf16 v[116:119], v[146:149], v[172:175], v[116:119]
	v_mfma_f32_16x16x32_bf16 v[112:115], v[154:157], v[172:175], v[112:115]
	v_mfma_f32_16x16x32_bf16 v[84:87], v[146:149], v[196:199], v[84:87]
	v_mfma_f32_16x16x32_bf16 v[80:83], v[154:157], v[196:199], v[80:83]
	v_mfma_f32_16x16x32_bf16 v[68:71], v[146:149], v[204:207], v[68:71]
	v_mfma_f32_16x16x32_bf16 v[64:67], v[154:157], v[204:207], v[64:67]
	v_mfma_f32_16x16x32_bf16 v[134:137], v[150:153], v[166:169], v[134:137]
	v_mfma_f32_16x16x32_bf16 v[130:133], v[158:161], v[166:169], v[130:133]
	v_mfma_f32_16x16x32_bf16 v[116:119], v[150:153], v[188:191], v[116:119]
	v_mfma_f32_16x16x32_bf16 v[112:115], v[158:161], v[188:191], v[112:115]
	v_mfma_f32_16x16x32_bf16 v[84:87], v[150:153], v[200:203], v[84:87]
	v_mfma_f32_16x16x32_bf16 v[80:83], v[158:161], v[200:203], v[80:83]
	v_mfma_f32_16x16x32_bf16 v[68:71], v[150:153], v[208:211], v[68:71]
	v_mfma_f32_16x16x32_bf16 v[64:67], v[158:161], v[208:211], v[64:67]
	s_barrier
; #define PG8_STAGE(bufoff, gbase, voff) do { _Pragma("unroll") for (int _i = 0; _i < 2; ++_i) \
;         __builtin_amdgcn_global_load_lds((const unsigned*)((const char*)(gbase) + (voff)[_i]), (PG8_LAS unsigned*)(lds + (bufoff) + ldsw + _i * 8192), 16, 0, 0); } while (0)
; #define PG8_LDA(dst, b, h) do { _Pragma("unroll") for (int m = 0; m < 4; ++m) _Pragma("unroll") for (int k = 0; k < 2; ++k) dst[m][k] = *(const PG8_LAS bf16x8*)(lds + PG8_SA(b, h) + aoff + m * 2048 + k * 1024); } while (0)
; #define PG8_MMA(ai, bj, At, Bt) do { __builtin_amdgcn_s_setprio(1); _Pragma("unroll") for (int m = 0; m < 4; ++m) _Pragma("unroll") for (int n = 0; n < 2; ++n) _Pragma("unroll") for (int k = 0; k < 2; ++k) \
;         acc[ai][bj][m][n] = __builtin_amdgcn_mfma_f32_16x16x32_bf16(Bt[n][k], At[m][k], acc[ai][bj][m][n], 0, 0, 0); __builtin_amdgcn_s_setprio(0); } while (0)
; #define PG8_WAIT_V(n) asm volatile("s_waitcnt vmcnt(" #n ")" ::: "memory")
; #define PG8_WAIT_L(n) asm volatile("s_waitcnt lgkmcnt(" #n ")" ::: "memory")
; #define PG8_BAR __builtin_amdgcn_s_barrier()
; #define PG8_SCHED __builtin_amdgcn_sched_barrier(0)
; template <class Epi, class Sched, bool ALIGN_EPI>
; __device__ __forceinline__ void gemm_phase(PG8_LAS unsigned char* lds, const Gemm g, const Sched& S, const Epi& E, const int tid) {
;     ...
;             PG8_LDA(At, 1, 1); PG8_STAGE(PG8_SB(1, 0), b3, voffB); PG8_STAGE(PG8_SB(1, 1), b3 + hstepB, voffB); PG8_STAGE(PG8_SA(1, 0), a3, voffA);
;             PG8_WAIT_V(8); PG8_WAIT_L(0); PG8_BAR; PG8_MMA(1, 0, At, B0); PG8_MMA(1, 1, At, B1); PG8_BAR; PG8_SCHED;
;         }
	s_setprio 0
	s_add_u32 s26, s24, 0x8000
	s_addc_u32 s27, s25, 0
	s_add_i32 s54, s54, s30
	v_lshl_add_u64 v[192:193], s[26:27], 0, v[178:179]
	s_mov_b32 m0, s54
	ds_read_b128 v[162:165], v185 offset:49152
	ds_read_b128 v[166:169], v185 offset:50176
	ds_read_b128 v[172:175], v185 offset:51200
	ds_read_b128 v[188:191], v185 offset:52224
	ds_read_b128 v[196:199], v185 offset:53248
	ds_read_b128 v[200:203], v185 offset:54272
	ds_read_b128 v[204:207], v185 offset:55296
	ds_read_b128 v[208:211], v185 offset:56320
	global_load_lds_dwordx4 v[192:193], off
	s_add_i32 m0, s54, 0x2000
	s_add_u32 s24, s24, 0xc000
	v_lshl_add_u64 v[192:193], s[26:27], 0, v[182:183]
	s_addc_u32 s25, s25, 0
	s_add_i32 s26, s55, s30
	global_load_lds_dwordx4 v[192:193], off
	v_lshl_add_u64 v[192:193], s[24:25], 0, v[178:179]
	s_mov_b32 m0, s26
	s_nop 0
	global_load_lds_dwordx4 v[192:193], off
	v_lshl_add_u64 v[192:193], s[24:25], 0, v[182:183]
	s_add_i32 m0, s26, 0x2000
	s_nop 0
	global_load_lds_dwordx4 v[192:193], off
	v_lshl_add_u64 v[192:193], s[20:21], 0, v[176:177]
	s_mov_b32 m0, s40
	s_nop 0
	global_load_lds_dwordx4 v[192:193], off
	v_lshl_add_u64 v[192:193], s[20:21], 0, v[180:181]
	s_mov_b32 m0, s41
	s_nop 0
	global_load_lds_dwordx4 v[192:193], off
	s_waitcnt vmcnt(8)
	s_waitcnt lgkmcnt(0)
	s_setprio 1
	s_barrier
	v_mfma_f32_16x16x32_bf16 v[60:63], v[88:91], v[162:165], v[60:63]
	v_mfma_f32_16x16x32_bf16 v[56:59], v[100:103], v[162:165], v[56:59]
	v_mfma_f32_16x16x32_bf16 v[44:47], v[88:91], v[172:175], v[44:47]
	v_mfma_f32_16x16x32_bf16 v[40:43], v[100:103], v[172:175], v[40:43]
	v_mfma_f32_16x16x32_bf16 v[28:31], v[88:91], v[196:199], v[28:31]
	v_mfma_f32_16x16x32_bf16 v[24:27], v[100:103], v[196:199], v[24:27]
	v_mfma_f32_16x16x32_bf16 v[12:15], v[88:91], v[204:207], v[12:15]
	v_mfma_f32_16x16x32_bf16 v[8:11], v[100:103], v[204:207], v[8:11]
	v_mfma_f32_16x16x32_bf16 v[60:63], v[92:95], v[166:169], v[60:63]
	v_mfma_f32_16x16x32_bf16 v[56:59], v[108:111], v[166:169], v[56:59]
	v_mfma_f32_16x16x32_bf16 v[44:47], v[92:95], v[188:191], v[44:47]
	v_mfma_f32_16x16x32_bf16 v[40:43], v[108:111], v[188:191], v[40:43]
	v_mfma_f32_16x16x32_bf16 v[28:31], v[92:95], v[200:203], v[28:31]
	v_mfma_f32_16x16x32_bf16 v[24:27], v[108:111], v[200:203], v[24:27]
	v_mfma_f32_16x16x32_bf16 v[12:15], v[92:95], v[208:211], v[12:15]
	v_mfma_f32_16x16x32_bf16 v[8:11], v[108:111], v[208:211], v[8:11]
	v_mfma_f32_16x16x32_bf16 v[52:55], v[146:149], v[162:165], v[52:55]
	v_mfma_f32_16x16x32_bf16 v[48:51], v[154:157], v[162:165], v[48:51]
	v_mfma_f32_16x16x32_bf16 v[36:39], v[146:149], v[172:175], v[36:39]
	v_mfma_f32_16x16x32_bf16 v[32:35], v[154:157], v[172:175], v[32:35]
	v_mfma_f32_16x16x32_bf16 v[20:23], v[146:149], v[196:199], v[20:23]
	v_mfma_f32_16x16x32_bf16 v[16:19], v[154:157], v[196:199], v[16:19]
	v_mfma_f32_16x16x32_bf16 v[4:7], v[146:149], v[204:207], v[4:7]
	v_mfma_f32_16x16x32_bf16 v[0:3], v[154:157], v[204:207], v[0:3]
	v_mfma_f32_16x16x32_bf16 v[52:55], v[150:153], v[166:169], v[52:55]
	v_mfma_f32_16x16x32_bf16 v[48:51], v[158:161], v[166:169], v[48:51]
	v_mfma_f32_16x16x32_bf16 v[36:39], v[150:153], v[188:191], v[36:39]
	v_mfma_f32_16x16x32_bf16 v[32:35], v[158:161], v[188:191], v[32:35]
	v_mfma_f32_16x16x32_bf16 v[20:23], v[150:153], v[200:203], v[20:23]
	v_mfma_f32_16x16x32_bf16 v[16:19], v[158:161], v[200:203], v[16:19]
	v_mfma_f32_16x16x32_bf16 v[4:7], v[150:153], v[208:211], v[4:7]
	v_mfma_f32_16x16x32_bf16 v[0:3], v[158:161], v[208:211], v[0:3]
	s_barrier
	s_setprio 0
	s_add_u32 s52, s52, 0x10000
	s_addc_u32 s53, s53, 0
	s_cmp_ge_u32 s22, s37
	s_mov_b64 s[20:21], s[22:23]
	s_cbranch_scc0 .LBB0_1396
	s_and_b64 vcc, exec, s[14:15]
	s_cbranch_vccz .LBB0_1399
	s_barrier
